# conversion work re-split (P2 takes 2048 more W2 items from P4), GEMM M-seg head trimmed (setprio before barrier, redundant lgkmcnt wait and mid setprio toggles removed), false vmcnt(0) before transpos
# speedup vs baseline: 1.0126x; 1.0110x over previous
; #define PG8_STAGE(bufoff, gbase, voff) do { _Pragma("unroll") for (int _i = 0; _i < 2; ++_i) \
;         __builtin_amdgcn_global_load_lds((const unsigned*)((const char*)(gbase) + (voff)[_i]), (LAS unsigned*)(lds + (bufoff) + ldsw + _i * 8192), 16, 0, 0); } while (0)
; #define PG8_LDA(dst, b, h) do { if constexpr (FP8) { _Pragma("unroll") for (int m = 0; m < 4; ++m) dst##8[m] = PG8_LD8(lds + PG8_SA(b, h) + aoff + m * 2048); } \
;         else { _Pragma("unroll") for (int m = 0; m < 4; ++m) _Pragma("unroll") for (int k = 0; k < 2; ++k) dst[m][k] = *(const LAS bf16x8*)(lds + PG8_SA(b, h) + aoff + m * 2048 + k * 1024); } } while (0)
; #define PG8_LDB(dst, b, h) do { if constexpr (FP8) { _Pragma("unroll") for (int n = 0; n < 2; ++n) dst##8[n] = PG8_LD8(lds + PG8_SB(b, h) + boff + n * 2048); } \
;         else { _Pragma("unroll") for (int n = 0; n < 2; ++n) _Pragma("unroll") for (int k = 0; k < 2; ++k) dst[n][k] = *(const LAS bf16x8*)(lds + PG8_SB(b, h) + boff + n * 2048 + k * 1024); } } while (0)
; #define PG8_WAIT_V(n) asm volatile("s_waitcnt vmcnt(" #n ")" ::: "memory")
; #define PG8_WAIT_L(n) asm volatile("s_waitcnt lgkmcnt(" #n ")" ::: "memory")
; template <class Epi, class Sched, bool ALIGN_EPI, bool SP2, bool FP8 = false>
; __device__ __forceinline__ void gemm_phase(LAS unsigned char* lds, const int K, const Sched& S, const Epi& E) {
;     ...
;         for (int t = 0; t < nt; t += 2) {
;             const bool last = (t == nt - 2);
;             const char* a1 = cA + (size_t)(t + 1) * kstep;
;             const char* a2 = last ? nA : cA + (size_t)(t + 2) * kstep; const char* b2 = last ? nB : cB + (size_t)(t + 2) * kstep;
;             const char* a3 = a2 + kstep; const char* b3 = b2 + kstep;
;             unsigned vX0[2], vX1[2];
; #pragma unroll
;             for (int i = 0; i < 2; ++i) { vX0[i] = last ? vAn[0][i] : vAc[0][i]; vX1[i] = last ? vAn[1][i] : vAc[1][i]; }
;             PG8_LDB(B0, 0, 0); PG8_LDB(B1, 0, 1); PG8_SCHED; PG8_LDA(At, 0, 0); PG8_STAGE(PG8_SA(1, 1), a1, vAc[1]);
;             PG8_WAIT_V(8); PG8_WAIT_L(0); PG8_BAR; PG8_MMA(0, 0, At, B0); PG8_MMA(0, 1, At, B1); PG8_BAR; PG8_SCHED;
;             PG8_LDA(At, 0, 1); PG8_STAGE(PG8_SB(0, 0), b2, voffB); PG8_STAGE(PG8_SB(0, 1), b2 + hstep, voffB); PG8_STAGE(PG8_SA(0, 0), a2, vX0);
;             PG8_WAIT_V(8); PG8_WAIT_L(0); PG8_BAR; PG8_MMA(1, 0, At, B0); PG8_MMA(1, 1, At, B1); PG8_BAR; PG8_SCHED;
.LBB0_203:
	s_add_u32 s70, s4, s68
	s_addc_u32 s71, s5, s69
	v_add_u32_e32 v145, s87, v167
	s_add_u32 s72, s70, 0x100
	ds_read_b128 v[154:157], v183
	ds_read_b128 v[158:161], v183 offset:1024
	ds_read_b128 v[192:195], v183 offset:2048
	ds_read_b128 v[196:199], v183 offset:3072
	ds_read_b128 v[200:203], v145
	ds_read_b128 v[204:207], v145 offset:1024
	ds_read_b128 v[208:211], v145 offset:2048
	ds_read_b128 v[212:215], v145 offset:3072
	s_addc_u32 s73, s71, 0
	s_add_u32 s82, s45, s68
	s_addc_u32 s83, s96, s69
	s_cmpk_eq_i32 s68, 0xf00
	s_cselect_b64 vcc, -1, 0
	s_and_b64 s[70:71], vcc, exec
	v_cndmask_b32_e32 v136, v144, v186, vcc
	s_cselect_b32 s73, s63, s73
	s_cselect_b32 s72, s62, s72
	v_cndmask_b32_e32 v143, v142, v187, vcc
	v_cndmask_b32_e32 v162, v148, v188, vcc
	v_cndmask_b32_e32 v145, v146, v189, vcc
	s_cselect_b32 s71, s65, s83
	s_cselect_b32 s70, s64, s82
	v_lshl_add_u64 v[248:249], v[152:153], 0, s[68:69]
	s_add_i32 m0, s67, 0xc000
	ds_read_b128 v[216:219], v184
	ds_read_b128 v[220:223], v184 offset:1024
	ds_read_b128 v[224:227], v184 offset:2048
	ds_read_b128 v[228:231], v184 offset:3072
	ds_read_b128 v[232:235], v184 offset:4096
	ds_read_b128 v[236:239], v184 offset:5120
	ds_read_b128 v[240:243], v184 offset:6144
	ds_read_b128 v[244:247], v184 offset:7168
	global_load_lds_dwordx4 v[248:249], off
	v_lshl_add_u64 v[248:249], v[150:151], 0, s[68:69]
	s_add_i32 m0, s67, 0xe000
	s_nop 0
	global_load_lds_dwordx4 v[248:249], off
	s_waitcnt vmcnt(8)
	s_waitcnt lgkmcnt(0)
	s_setprio 1
	s_barrier
	v_mfma_f32_16x16x32_bf16 v[62:65], v[154:157], v[216:219], v[62:65]
	v_mfma_f32_16x16x32_bf16 v[58:61], v[192:195], v[216:219], v[58:61]
	v_mfma_f32_16x16x32_bf16 v[54:57], v[154:157], v[224:227], v[54:57]
	v_mfma_f32_16x16x32_bf16 v[50:53], v[192:195], v[224:227], v[50:53]
	v_mfma_f32_16x16x32_bf16 v[46:49], v[154:157], v[232:235], v[46:49]
	v_mfma_f32_16x16x32_bf16 v[42:45], v[192:195], v[232:235], v[42:45]
	v_mfma_f32_16x16x32_bf16 v[38:41], v[154:157], v[240:243], v[38:41]
	v_mfma_f32_16x16x32_bf16 v[34:37], v[192:195], v[240:243], v[34:37]
	v_mfma_f32_16x16x32_bf16 v[62:65], v[158:161], v[220:223], v[62:65]
	v_mfma_f32_16x16x32_bf16 v[58:61], v[196:199], v[220:223], v[58:61]
	v_mfma_f32_16x16x32_bf16 v[54:57], v[158:161], v[228:231], v[54:57]
	v_mfma_f32_16x16x32_bf16 v[50:53], v[196:199], v[228:231], v[50:53]
	v_mfma_f32_16x16x32_bf16 v[46:49], v[158:161], v[236:239], v[46:49]
	v_mfma_f32_16x16x32_bf16 v[42:45], v[196:199], v[236:239], v[42:45]
	v_mfma_f32_16x16x32_bf16 v[38:41], v[158:161], v[244:247], v[38:41]
	v_mfma_f32_16x16x32_bf16 v[34:37], v[196:199], v[244:247], v[34:37]
	v_mfma_f32_16x16x32_bf16 v[126:129], v[200:203], v[216:219], v[126:129]
	v_mfma_f32_16x16x32_bf16 v[122:125], v[208:211], v[216:219], v[122:125]
	v_mfma_f32_16x16x32_bf16 v[118:121], v[200:203], v[224:227], v[118:121]
	v_mfma_f32_16x16x32_bf16 v[114:117], v[208:211], v[224:227], v[114:117]
	v_mfma_f32_16x16x32_bf16 v[110:113], v[200:203], v[232:235], v[110:113]
	v_mfma_f32_16x16x32_bf16 v[106:109], v[208:211], v[232:235], v[106:109]
	v_mfma_f32_16x16x32_bf16 v[102:105], v[200:203], v[240:243], v[102:105]
	v_mfma_f32_16x16x32_bf16 v[98:101], v[208:211], v[240:243], v[98:101]
	v_mfma_f32_16x16x32_bf16 v[126:129], v[204:207], v[220:223], v[126:129]
	v_mfma_f32_16x16x32_bf16 v[122:125], v[212:215], v[220:223], v[122:125]
	v_mfma_f32_16x16x32_bf16 v[118:121], v[204:207], v[228:231], v[118:121]
	v_mfma_f32_16x16x32_bf16 v[114:117], v[212:215], v[228:231], v[114:117]
	v_mfma_f32_16x16x32_bf16 v[110:113], v[204:207], v[236:239], v[110:113]
	v_mfma_f32_16x16x32_bf16 v[106:109], v[212:215], v[236:239], v[106:109]
	v_mfma_f32_16x16x32_bf16 v[102:105], v[204:207], v[244:247], v[102:105]
	v_mfma_f32_16x16x32_bf16 v[98:101], v[212:215], v[244:247], v[98:101]
	s_setprio 0
	s_barrier
	s_add_i32 s82, s86, s74
	v_lshl_add_u64 v[248:249], s[70:71], 0, v[132:133]
	s_mov_b32 m0, s82
	ds_read_b128 v[216:219], v184 offset:16384
	ds_read_b128 v[220:223], v184 offset:17408
	ds_read_b128 v[224:227], v184 offset:18432
	ds_read_b128 v[228:231], v184 offset:19456
	ds_read_b128 v[232:235], v184 offset:20480
	ds_read_b128 v[236:239], v184 offset:21504
	ds_read_b128 v[240:243], v184 offset:22528
	ds_read_b128 v[244:247], v184 offset:23552
	global_load_lds_dwordx4 v[248:249], off
	s_add_i32 m0, s82, 0x2000
	s_add_u32 vcc_lo, s70, 0x80000
	v_lshl_add_u64 v[250:251], s[70:71], 0, v[134:135]
	s_addc_u32 vcc_hi, s71, 0
	s_add_i32 s82, s87, s74
	global_load_lds_dwordx4 v[250:251], off
	v_lshl_add_u64 v[252:253], vcc, 0, v[132:133]
	s_mov_b32 m0, s82
	v_mov_b32_e32 v163, v137
	global_load_lds_dwordx4 v[252:253], off
	v_lshl_add_u64 v[252:253], vcc, 0, v[134:135]
	s_add_i32 m0, s82, 0x2000
	s_nop 0
	global_load_lds_dwordx4 v[252:253], off
	s_mov_b32 m0, s67
	v_lshl_add_u64 v[252:253], s[72:73], 0, v[136:137]
	global_load_lds_dwordx4 v136, s[72:73]
	s_mov_b32 m0, s75
	s_nop 0
	global_load_lds_dwordx4 v162, s[72:73]
	s_waitcnt vmcnt(8)
	s_waitcnt lgkmcnt(0)
	v_lshl_add_u64 v[162:163], s[72:73], 0, v[162:163]
	s_setprio 1
	s_barrier
; #define PG8_STAGE(bufoff, gbase, voff) do { _Pragma("unroll") for (int _i = 0; _i < 2; ++_i) \
;         __builtin_amdgcn_global_load_lds((const unsigned*)((const char*)(gbase) + (voff)[_i]), (LAS unsigned*)(lds + (bufoff) + ldsw + _i * 8192), 16, 0, 0); } while (0)
; #define PG8_LDA(dst, b, h) do { if constexpr (FP8) { _Pragma("unroll") for (int m = 0; m < 4; ++m) dst##8[m] = PG8_LD8(lds + PG8_SA(b, h) + aoff + m * 2048); } \
;         else { _Pragma("unroll") for (int m = 0; m < 4; ++m) _Pragma("unroll") for (int k = 0; k < 2; ++k) dst[m][k] = *(const LAS bf16x8*)(lds + PG8_SA(b, h) + aoff + m * 2048 + k * 1024); } } while (0)
; #define PG8_LDB(dst, b, h) do { if constexpr (FP8) { _Pragma("unroll") for (int n = 0; n < 2; ++n) dst##8[n] = PG8_LD8(lds + PG8_SB(b, h) + boff + n * 2048); } \
;         else { _Pragma("unroll") for (int n = 0; n < 2; ++n) _Pragma("unroll") for (int k = 0; k < 2; ++k) dst[n][k] = *(const LAS bf16x8*)(lds + PG8_SB(b, h) + boff + n * 2048 + k * 1024); } } while (0)
; #define PG8_WAIT_V(n) asm volatile("s_waitcnt vmcnt(" #n ")" ::: "memory")
; #define PG8_WAIT_L(n) asm volatile("s_waitcnt lgkmcnt(" #n ")" ::: "memory")
; #define PG8_BAR __builtin_amdgcn_s_barrier()
; #define PG8_SCHED __builtin_amdgcn_sched_barrier(0)
; template <class Epi, class Sched, bool ALIGN_EPI, bool SP2, bool FP8 = false>
; __device__ __forceinline__ void gemm_phase(LAS unsigned char* lds, const int K, const Sched& S, const Epi& E) {
;     ...
;             PG8_WAIT_V(8); PG8_WAIT_L(0); PG8_BAR; PG8_MMA(1, 0, At, B0); PG8_MMA(1, 1, At, B1); PG8_BAR; PG8_SCHED;
;             PG8_LDB(B0, 1, 0); PG8_LDB(B1, 1, 1); PG8_SCHED; PG8_LDA(At, 1, 0); PG8_STAGE(PG8_SA(0, 1), a2, vX1);
;             PG8_WAIT_V(8); PG8_WAIT_L(0); PG8_BAR; PG8_MMA(0, 0, At, B0); PG8_MMA(0, 1, At, B1); PG8_BAR; PG8_SCHED;
	v_mfma_f32_16x16x32_bf16 v[30:33], v[154:157], v[216:219], v[30:33]
	v_mfma_f32_16x16x32_bf16 v[26:29], v[192:195], v[216:219], v[26:29]
	v_mfma_f32_16x16x32_bf16 v[22:25], v[154:157], v[224:227], v[22:25]
	v_mfma_f32_16x16x32_bf16 v[18:21], v[192:195], v[224:227], v[18:21]
	v_mfma_f32_16x16x32_bf16 v[14:17], v[154:157], v[232:235], v[14:17]
	v_mfma_f32_16x16x32_bf16 v[10:13], v[192:195], v[232:235], v[10:13]
	v_mfma_f32_16x16x32_bf16 v[6:9], v[154:157], v[240:243], v[6:9]
	v_mfma_f32_16x16x32_bf16 v[2:5], v[192:195], v[240:243], v[2:5]
	v_mfma_f32_16x16x32_bf16 v[30:33], v[158:161], v[220:223], v[30:33]
	v_mfma_f32_16x16x32_bf16 v[26:29], v[196:199], v[220:223], v[26:29]
	v_mfma_f32_16x16x32_bf16 v[22:25], v[158:161], v[228:231], v[22:25]
	v_mfma_f32_16x16x32_bf16 v[18:21], v[196:199], v[228:231], v[18:21]
	v_mfma_f32_16x16x32_bf16 v[14:17], v[158:161], v[236:239], v[14:17]
	v_mfma_f32_16x16x32_bf16 v[10:13], v[196:199], v[236:239], v[10:13]
	v_mfma_f32_16x16x32_bf16 v[6:9], v[158:161], v[244:247], v[6:9]
	v_mfma_f32_16x16x32_bf16 v[2:5], v[196:199], v[244:247], v[2:5]
	v_mfma_f32_16x16x32_bf16 v[94:97], v[200:203], v[216:219], v[94:97]
	v_mfma_f32_16x16x32_bf16 v[90:93], v[208:211], v[216:219], v[90:93]
	v_mfma_f32_16x16x32_bf16 v[86:89], v[200:203], v[224:227], v[86:89]
	v_mfma_f32_16x16x32_bf16 v[82:85], v[208:211], v[224:227], v[82:85]
	v_mfma_f32_16x16x32_bf16 v[78:81], v[200:203], v[232:235], v[78:81]
	v_mfma_f32_16x16x32_bf16 v[74:77], v[208:211], v[232:235], v[74:77]
	v_mfma_f32_16x16x32_bf16 v[66:69], v[200:203], v[240:243], v[66:69]
	v_mfma_f32_16x16x32_bf16 v[70:73], v[208:211], v[240:243], v[70:73]
	v_mfma_f32_16x16x32_bf16 v[94:97], v[204:207], v[220:223], v[94:97]
	v_mfma_f32_16x16x32_bf16 v[90:93], v[212:215], v[220:223], v[90:93]
	v_mfma_f32_16x16x32_bf16 v[86:89], v[204:207], v[228:231], v[86:89]
	v_mfma_f32_16x16x32_bf16 v[82:85], v[212:215], v[228:231], v[82:85]
	v_mfma_f32_16x16x32_bf16 v[78:81], v[204:207], v[236:239], v[78:81]
	v_mfma_f32_16x16x32_bf16 v[74:77], v[212:215], v[236:239], v[74:77]
	v_mfma_f32_16x16x32_bf16 v[66:69], v[204:207], v[244:247], v[66:69]
	v_mfma_f32_16x16x32_bf16 v[70:73], v[212:215], v[244:247], v[70:73]
	s_setprio 0
	s_barrier
	s_add_i32 s82, 0, 0x18000
	v_add_u32_e32 v136, s82, v167
	s_add_i32 s83, 0, 0x1c000
	ds_read_b128 v[154:157], v136
	ds_read_b128 v[158:161], v136 offset:1024
	ds_read_b128 v[192:195], v136 offset:2048
	ds_read_b128 v[196:199], v136 offset:3072
	v_add_u32_e32 v136, s83, v167
	ds_read_b128 v[200:203], v136
	ds_read_b128 v[204:207], v136 offset:1024
	ds_read_b128 v[208:211], v136 offset:2048
	ds_read_b128 v[212:215], v136 offset:3072
	s_mov_b32 m0, s76
	ds_read_b128 v[216:219], v184 offset:32768
	ds_read_b128 v[220:223], v184 offset:33792
	ds_read_b128 v[224:227], v184 offset:34816
	ds_read_b128 v[228:231], v184 offset:35840
	ds_read_b128 v[232:235], v184 offset:36864
	ds_read_b128 v[236:239], v184 offset:37888
	ds_read_b128 v[240:243], v184 offset:38912
	ds_read_b128 v[244:247], v184 offset:39936
	global_load_lds_dwordx4 v143, s[72:73]
	s_mov_b32 m0, s77
	s_nop 0
	global_load_lds_dwordx4 v145, s[72:73]
	s_waitcnt vmcnt(8)
	s_waitcnt lgkmcnt(0)
	s_setprio 1
	s_barrier
	v_mfma_f32_16x16x32_bf16 v[62:65], v[154:157], v[216:219], v[62:65]
	v_mfma_f32_16x16x32_bf16 v[58:61], v[192:195], v[216:219], v[58:61]
	v_mfma_f32_16x16x32_bf16 v[54:57], v[154:157], v[224:227], v[54:57]
	v_mfma_f32_16x16x32_bf16 v[50:53], v[192:195], v[224:227], v[50:53]
	v_mfma_f32_16x16x32_bf16 v[46:49], v[154:157], v[232:235], v[46:49]
	v_mfma_f32_16x16x32_bf16 v[42:45], v[192:195], v[232:235], v[42:45]
	v_mfma_f32_16x16x32_bf16 v[38:41], v[154:157], v[240:243], v[38:41]
	v_mfma_f32_16x16x32_bf16 v[34:37], v[192:195], v[240:243], v[34:37]
	v_mfma_f32_16x16x32_bf16 v[62:65], v[158:161], v[220:223], v[62:65]
	v_mfma_f32_16x16x32_bf16 v[58:61], v[196:199], v[220:223], v[58:61]
	v_mfma_f32_16x16x32_bf16 v[54:57], v[158:161], v[228:231], v[54:57]
	v_mfma_f32_16x16x32_bf16 v[50:53], v[196:199], v[228:231], v[50:53]
	v_mfma_f32_16x16x32_bf16 v[46:49], v[158:161], v[236:239], v[46:49]
	v_mfma_f32_16x16x32_bf16 v[42:45], v[196:199], v[236:239], v[42:45]
	v_mfma_f32_16x16x32_bf16 v[38:41], v[158:161], v[244:247], v[38:41]
	v_mfma_f32_16x16x32_bf16 v[34:37], v[196:199], v[244:247], v[34:37]
	v_mfma_f32_16x16x32_bf16 v[126:129], v[200:203], v[216:219], v[126:129]
	v_mfma_f32_16x16x32_bf16 v[122:125], v[208:211], v[216:219], v[122:125]
	v_mfma_f32_16x16x32_bf16 v[118:121], v[200:203], v[224:227], v[118:121]
	v_mfma_f32_16x16x32_bf16 v[114:117], v[208:211], v[224:227], v[114:117]
	v_mfma_f32_16x16x32_bf16 v[110:113], v[200:203], v[232:235], v[110:113]
	v_mfma_f32_16x16x32_bf16 v[106:109], v[208:211], v[232:235], v[106:109]
	v_mfma_f32_16x16x32_bf16 v[102:105], v[200:203], v[240:243], v[102:105]
	v_mfma_f32_16x16x32_bf16 v[98:101], v[208:211], v[240:243], v[98:101]
	v_mfma_f32_16x16x32_bf16 v[126:129], v[204:207], v[220:223], v[126:129]
	v_mfma_f32_16x16x32_bf16 v[122:125], v[212:215], v[220:223], v[122:125]
	v_mfma_f32_16x16x32_bf16 v[118:121], v[204:207], v[228:231], v[118:121]
	v_mfma_f32_16x16x32_bf16 v[114:117], v[212:215], v[228:231], v[114:117]
	v_mfma_f32_16x16x32_bf16 v[110:113], v[204:207], v[236:239], v[110:113]
	v_mfma_f32_16x16x32_bf16 v[106:109], v[212:215], v[236:239], v[106:109]
	v_mfma_f32_16x16x32_bf16 v[102:105], v[204:207], v[244:247], v[102:105]
	v_mfma_f32_16x16x32_bf16 v[98:101], v[212:215], v[244:247], v[98:101]
	s_setprio 0
	s_barrier
; #define PG8_STAGE(bufoff, gbase, voff) do { _Pragma("unroll") for (int _i = 0; _i < 2; ++_i) \
;         __builtin_amdgcn_global_load_lds((const unsigned*)((const char*)(gbase) + (voff)[_i]), (LAS unsigned*)(lds + (bufoff) + ldsw + _i * 8192), 16, 0, 0); } while (0)
; #define PG8_LDA(dst, b, h) do { if constexpr (FP8) { _Pragma("unroll") for (int m = 0; m < 4; ++m) dst##8[m] = PG8_LD8(lds + PG8_SA(b, h) + aoff + m * 2048); } \
;         else { _Pragma("unroll") for (int m = 0; m < 4; ++m) _Pragma("unroll") for (int k = 0; k < 2; ++k) dst[m][k] = *(const LAS bf16x8*)(lds + PG8_SA(b, h) + aoff + m * 2048 + k * 1024); } } while (0)
; #define PG8_WAIT_V(n) asm volatile("s_waitcnt vmcnt(" #n ")" ::: "memory")
; #define PG8_WAIT_L(n) asm volatile("s_waitcnt lgkmcnt(" #n ")" ::: "memory")
; #define PG8_BAR __builtin_amdgcn_s_barrier()
; #define PG8_SCHED __builtin_amdgcn_sched_barrier(0)
; template <class Epi, class Sched, bool ALIGN_EPI, bool SP2, bool FP8 = false>
; __device__ __forceinline__ void gemm_phase(LAS unsigned char* lds, const int K, const Sched& S, const Epi& E) {
;     ...
;             PG8_LDA(At, 1, 1); PG8_STAGE(PG8_SB(1, 0), b3, voffB); PG8_STAGE(PG8_SB(1, 1), b3 + hstep, voffB); PG8_STAGE(PG8_SA(1, 0), a3, vX0);
;             PG8_WAIT_V(8); PG8_WAIT_L(0); PG8_BAR; PG8_MMA(1, 0, At, B0); PG8_MMA(1, 1, At, B1); PG8_BAR; PG8_SCHED;
;         }
;         if constexpr (ALIGN_EPI) { if (wr == 0) PG8_BAR; }
	s_add_i32 s72, s82, s74
	v_lshl_add_u64 v[248:249], v[248:249], 0, s[50:51]
	s_mov_b32 m0, s72
	ds_read_b128 v[216:219], v184 offset:49152
	ds_read_b128 v[220:223], v184 offset:50176
	ds_read_b128 v[224:227], v184 offset:51200
	ds_read_b128 v[228:231], v184 offset:52224
	ds_read_b128 v[232:235], v184 offset:53248
	ds_read_b128 v[236:239], v184 offset:54272
	ds_read_b128 v[240:243], v184 offset:55296
	ds_read_b128 v[244:247], v184 offset:56320
	global_load_lds_dwordx4 v[248:249], off
	s_add_i32 m0, s72, 0x2000
	s_add_u32 s70, s70, 0x80080
	v_lshl_add_u64 v[248:249], v[250:251], 0, s[50:51]
	s_addc_u32 s71, s71, 0
	s_add_i32 s72, s83, s74
	global_load_lds_dwordx4 v[248:249], off
	v_lshl_add_u64 v[248:249], s[70:71], 0, v[132:133]
	s_mov_b32 m0, s72
	v_lshl_add_u64 v[162:163], v[162:163], 0, s[50:51]
	global_load_lds_dwordx4 v[248:249], off
	v_lshl_add_u64 v[248:249], s[70:71], 0, v[134:135]
	s_add_i32 m0, s72, 0x2000
	s_nop 0
	global_load_lds_dwordx4 v[248:249], off
	v_lshl_add_u64 v[248:249], v[252:253], 0, s[50:51]
	s_mov_b32 m0, s79
	s_nop 0
	global_load_lds_dwordx4 v[248:249], off
	s_mov_b32 m0, s80
	s_nop 0
	global_load_lds_dwordx4 v[162:163], off
	s_waitcnt vmcnt(8)
	s_waitcnt lgkmcnt(0)
	s_setprio 1
	s_barrier
	v_mfma_f32_16x16x32_bf16 v[30:33], v[154:157], v[216:219], v[30:33]
	v_mfma_f32_16x16x32_bf16 v[26:29], v[192:195], v[216:219], v[26:29]
	v_mfma_f32_16x16x32_bf16 v[22:25], v[154:157], v[224:227], v[22:25]
	v_mfma_f32_16x16x32_bf16 v[18:21], v[192:195], v[224:227], v[18:21]
	v_mfma_f32_16x16x32_bf16 v[14:17], v[154:157], v[232:235], v[14:17]
	v_mfma_f32_16x16x32_bf16 v[10:13], v[192:195], v[232:235], v[10:13]
	v_mfma_f32_16x16x32_bf16 v[6:9], v[154:157], v[240:243], v[6:9]
	v_mfma_f32_16x16x32_bf16 v[2:5], v[192:195], v[240:243], v[2:5]
	v_mfma_f32_16x16x32_bf16 v[30:33], v[158:161], v[220:223], v[30:33]
	v_mfma_f32_16x16x32_bf16 v[26:29], v[196:199], v[220:223], v[26:29]
	v_mfma_f32_16x16x32_bf16 v[22:25], v[158:161], v[228:231], v[22:25]
	v_mfma_f32_16x16x32_bf16 v[18:21], v[196:199], v[228:231], v[18:21]
	v_mfma_f32_16x16x32_bf16 v[14:17], v[158:161], v[236:239], v[14:17]
	v_mfma_f32_16x16x32_bf16 v[10:13], v[196:199], v[236:239], v[10:13]
	v_mfma_f32_16x16x32_bf16 v[6:9], v[158:161], v[244:247], v[6:9]
	v_mfma_f32_16x16x32_bf16 v[2:5], v[196:199], v[244:247], v[2:5]
	v_mfma_f32_16x16x32_bf16 v[94:97], v[200:203], v[216:219], v[94:97]
	v_mfma_f32_16x16x32_bf16 v[90:93], v[208:211], v[216:219], v[90:93]
	v_mfma_f32_16x16x32_bf16 v[86:89], v[200:203], v[224:227], v[86:89]
	v_mfma_f32_16x16x32_bf16 v[82:85], v[208:211], v[224:227], v[82:85]
	v_mfma_f32_16x16x32_bf16 v[78:81], v[200:203], v[232:235], v[78:81]
	v_mfma_f32_16x16x32_bf16 v[74:77], v[208:211], v[232:235], v[74:77]
	v_mfma_f32_16x16x32_bf16 v[66:69], v[200:203], v[240:243], v[66:69]
	v_mfma_f32_16x16x32_bf16 v[70:73], v[208:211], v[240:243], v[70:73]
	v_mfma_f32_16x16x32_bf16 v[94:97], v[204:207], v[220:223], v[94:97]
	v_mfma_f32_16x16x32_bf16 v[90:93], v[212:215], v[220:223], v[90:93]
	v_mfma_f32_16x16x32_bf16 v[86:89], v[204:207], v[228:231], v[86:89]
	v_mfma_f32_16x16x32_bf16 v[82:85], v[212:215], v[228:231], v[82:85]
	v_mfma_f32_16x16x32_bf16 v[78:81], v[204:207], v[236:239], v[78:81]
	v_mfma_f32_16x16x32_bf16 v[74:77], v[212:215], v[236:239], v[74:77]
	v_mfma_f32_16x16x32_bf16 v[66:69], v[204:207], v[244:247], v[66:69]
	v_mfma_f32_16x16x32_bf16 v[70:73], v[212:215], v[244:247], v[70:73]
	s_setprio 0
	s_barrier
	s_add_i32 s97, s97, 2
	s_add_u32 s68, s68, 0x100
	s_addc_u32 s69, s69, 0
	s_cmp_gt_u32 s97, 29
	s_cbranch_scc0 .LBB0_203
	s_and_b64 vcc, exec, s[58:59]
	s_cbranch_vccz .LBB0_206
	s_barrier

; #define LAS __attribute__((address_space(3)))
; __device__ __forceinline__ void cvt_fill_g(const Frame& F) { LAS float* gl = (LAS float*)(F.lds + BG_G_OFF); for (int i = F.tid; i < DM; i += NTHREADS) gl[i] = F.g_moe[i] * WSCALE; __syncthreads(); }
;     __device__ __forceinline__ void init(const Frame& F_, int first_item, int n_items) { init(F_, first_item, n_items, F_.vcu, F_.G); }
; __global__ void __launch_bounds__(NTHREADS, 2) mk_fwd(Args args) {
;     ...
;         cvt_fill_g(F);
;         Bg bg; bg.init(F, CVT_P0_ITEMS, CVT_ITEMS - CVT_P0_ITEMS - (F.G == 256 ? CVT_P9_ITEMS + CVT_P4_ITEMS + CVT_P1_ITEMS : 0));
.LBB0_367:
	global_load_dword v5, v[2:3], off
	v_add_u32_e32 v4, 0x200, v4
	v_cmp_lt_u32_e32 vcc, s3, v4
	v_lshl_add_u64 v[2:3], v[2:3], 0, s[4:5]
	s_or_b64 s[0:1], vcc, s[0:1]
	s_waitcnt vmcnt(0)
	v_mul_f32_e32 v5, 0x42800000, v5
	ds_write_b32 v1, v5
	v_add_u32_e32 v1, 0x800, v1
	s_andn2_b64 exec, exec, s[0:1]
	s_cbranch_execnz .LBB0_367
	s_or_b64 exec, exec, s[0:1]
	s_cmpk_eq_i32 s33, 0x100
	s_movk_i32 s0, 0x4800
	v_readlane_b32 s1, v254, 8
	s_cselect_b32 s0, s0, 0x6000
	s_lshl_b32 s3, s52, 2
	s_lshr_b32 s1, s1, 7
	s_add_i32 s3, s3, s1
	s_addk_i32 s3, 0x800
	s_lshl_b32 s55, s33, 2
	s_cmp_ge_i32 s3, s0
	s_mov_b32 s54, 0
	s_waitcnt lgkmcnt(0)
	s_barrier
	s_cbranch_scc1 .LBB0_370
	s_abs_i32 s1, s55
	v_cvt_f32_u32_e32 v1, s1
	s_add_i32 s0, s55, s0
	s_not_b32 s4, s3
	s_add_i32 s4, s4, s0
	v_rcp_iflag_f32_e32 v1, v1
	s_sub_i32 s0, 0, s1
	s_xor_b32 s5, s4, s55
	s_abs_i32 s4, s4
	v_mul_f32_e32 v1, 0x4f7ffffe, v1
	v_cvt_u32_f32_e32 v1, v1
	s_ashr_i32 s5, s5, 31
	v_readfirstlane_b32 s6, v1
	s_mul_i32 s0, s0, s6
	s_mul_hi_u32 s0, s6, s0
	s_add_i32 s6, s6, s0
	s_mul_hi_u32 s0, s4, s6
	s_mul_i32 s6, s0, s1
	s_sub_i32 s4, s4, s6
	s_add_i32 s7, s0, 1
	s_sub_i32 s6, s4, s1
	s_cmp_ge_u32 s4, s1
	s_cselect_b32 s0, s7, s0
	s_cselect_b32 s4, s6, s4
	s_add_i32 s6, s0, 1
	s_cmp_ge_u32 s4, s1
	s_cselect_b32 s0, s6, s0
	s_xor_b32 s0, s0, s5
	s_sub_i32 s0, s0, s5
	s_lshl_b32 s54, s0, 1

; #define LAS __attribute__((address_space(3)))
; __device__ __forceinline__ unsigned cvtpk(float lo, float hi) { typedef __bf16 bf16x2_t __attribute__((ext_vector_type(2))); f32x2 v = {lo, hi}; bf16x2_t b = __builtin_convertvector(v, bf16x2_t); return __builtin_bit_cast(unsigned, b); }
; __device__ __forceinline__ s16x4 vtr(const LAS unsigned char* p) { return __builtin_bit_cast(s16x4, __builtin_amdgcn_ds_read_tr16_b64_v4i16((LAS v4i16_t*)p)); }
; template <int D, bool MASK, bool BIAS, bool SINK, bool REV, bool O8, class BG>
; __device__ __forceinline__ void attn_unit(const Prm& P, LAS unsigned char* lds, BG& bg) {
;     ...
;             float sacc = 0.f;
; #pragma unroll
;             for (int r = 0; r < 16; ++r) { p0[r] = __builtin_amdgcn_exp2f(p0[r]); p1[r] = __builtin_amdgcn_exp2f(p1[r]); sacc += p0[r] + p1[r]; }
;             l_reg += sacc;
;             u32x4 pw[4];
; #pragma unroll
;             for (int q = 0; q < 4; ++q) { pw[0][q] = cvtpk(p0[2 * q], p0[2 * q + 1]); pw[1][q] = cvtpk(p0[8 + 2 * q], p0[9 + 2 * q]); pw[2][q] = cvtpk(p1[2 * q], p1[2 * q + 1]); pw[3][q] = cvtpk(p1[8 + 2 * q], p1[9 + 2 * q]); }
;             const LAS unsigned char* vs = lds + VOFF + s * KSLOT + ((lane >> 4) & 1) * 32 + (lane & 3) * 8 + (4 * hi + ((lane & 15) >> 2)) * 64;
; #pragma unroll
;             for (int d = 0; d < NDB; ++d)
; #pragma unroll
;                 for (int k4 = 0; k4 < 4; ++k4) {
;                     const s16x4 vlo = vtr(vs + d * 4096 + k4 * 1024), vhi = vtr(vs + d * 4096 + k4 * 1024 + 512);
;                     const bf16x8 vf = (bf16x8){vlo[0], vlo[1], vlo[2], vlo[3], vhi[0], vhi[1], vhi[2], vhi[3]};
;                     o[d] = __builtin_amdgcn_mfma_f32_32x32x16_bf16(__builtin_bit_cast(bf16x8, pw[k4]), vf, o[d], 0, 0, 0);
;                 }
.LBB0_477:
	v_exp_f32_e32 v78, v2
	v_exp_f32_e32 v79, v64
	v_exp_f32_e32 v2, v1
	v_exp_f32_e32 v66, v65
	v_exp_f32_e32 v1, v58
	v_add_f32_e32 v67, v79, v78
	v_exp_f32_e32 v68, v63
	v_pk_add_f32 v[64:65], v[66:67], v[2:3]
	v_exp_f32_e32 v67, v62
	v_pk_add_f32 v[64:65], v[64:65], v[64:65] op_sel_hi:[0,1]
	v_exp_f32_e32 v64, v59
	v_exp_f32_e32 v62, v61
	v_add_f32_e32 v69, v67, v1
	v_exp_f32_e32 v42, v42
	v_pk_add_f32 v[58:59], v[68:69], v[64:65]
	v_exp_f32_e32 v65, v54
	v_pk_add_f32 v[58:59], v[58:59], v[58:59] op_sel_hi:[0,1]
	v_exp_f32_e32 v69, v60
	v_exp_f32_e32 v58, v55
	v_exp_f32_e32 v60, v57
	v_exp_f32_e32 v72, v45
	v_add_f32_e32 v63, v69, v65
	v_pk_add_f32 v[54:55], v[62:63], v[58:59]
	v_exp_f32_e32 v59, v50
	v_pk_add_f32 v[54:55], v[54:55], v[54:55] op_sel_hi:[0,1]
	v_exp_f32_e32 v63, v56
	v_exp_f32_e32 v54, v51
	v_exp_f32_e32 v56, v53
	v_exp_f32_e32 v76, v43
	v_add_f32_e32 v61, v63, v59
	v_pk_add_f32 v[50:51], v[60:61], v[54:55]
	v_exp_f32_e32 v55, v46
	v_pk_add_f32 v[50:51], v[50:51], v[50:51] op_sel_hi:[0,1]
	v_exp_f32_e32 v61, v52
	v_exp_f32_e32 v50, v47
	v_exp_f32_e32 v52, v49
	v_cvt_pk_bf16_f32 v43, v59, v54
	v_add_f32_e32 v57, v61, v55
	v_pk_add_f32 v[46:47], v[56:57], v[50:51]
	v_exp_f32_e32 v51, v48
	v_pk_add_f32 v[46:47], v[46:47], v[46:47] op_sel_hi:[0,1]
	v_exp_f32_e32 v46, v41
	v_exp_f32_e32 v57, v40
	v_add_f32_e32 v53, v51, v42
	v_cvt_pk_bf16_f32 v41, v1, v64
	v_pk_add_f32 v[48:49], v[52:53], v[46:47]
	v_exp_f32_e32 v47, v38
	v_pk_add_f32 v[70:71], v[48:49], v[48:49] op_sel_hi:[0,1]
	v_exp_f32_e32 v53, v44
	v_exp_f32_e32 v70, v39
	v_add_u32_e32 v1, s14, v194
	v_cvt_pk_bf16_f32 v40, v78, v2
	v_add_f32_e32 v73, v53, v47
	v_pk_add_f32 v[38:39], v[72:73], v[70:71]
	v_cvt_pk_bf16_f32 v44, v55, v50
	v_pk_add_f32 v[74:75], v[38:39], v[38:39] op_sel_hi:[0,1]
	v_exp_f32_e32 v39, v36
	v_exp_f32_e32 v74, v37
	v_cvt_pk_bf16_f32 v45, v42, v46
	v_cvt_pk_bf16_f32 v42, v65, v58
	v_add_f32_e32 v77, v57, v39
	v_pk_add_f32 v[36:37], v[76:77], v[74:75]
	v_cvt_pk_bf16_f32 v38, v53, v72
	v_add_f32_e32 v71, v36, v37
	v_cvt_pk_bf16_f32 v37, v51, v52
	s_nop 0
	ds_read_b64_tr_b16 v[52:53], v1 offset:32768
	ds_read_b64_tr_b16 v[54:55], v1 offset:33280
	s_waitcnt lgkmcnt(0)
	v_mfma_f32_32x32x16_bf16 v[4:19], v[40:43], v[52:55], v[4:19]
	v_cvt_pk_bf16_f32 v46, v47, v70
	v_cvt_pk_bf16_f32 v47, v39, v74
	ds_read_b64_tr_b16 v[52:53], v1 offset:33792
	ds_read_b64_tr_b16 v[54:55], v1 offset:34304
	v_cvt_pk_bf16_f32 v48, v79, v66
	v_cvt_pk_bf16_f32 v49, v67, v68
	v_cvt_pk_bf16_f32 v50, v69, v62
	v_cvt_pk_bf16_f32 v51, v63, v60
	s_waitcnt lgkmcnt(0)
	v_mfma_f32_32x32x16_bf16 v[4:19], v[44:47], v[52:55], v[4:19]
	ds_read_b64_tr_b16 v[52:53], v1 offset:34816
	ds_read_b64_tr_b16 v[54:55], v1 offset:35328
	v_cvt_pk_bf16_f32 v36, v61, v56
	v_cvt_pk_bf16_f32 v39, v57, v76
	v_add_f32_e32 v225, v225, v71
	s_mov_b64 s[92:93], 0
	s_waitcnt lgkmcnt(0)
	v_mfma_f32_32x32x16_bf16 v[4:19], v[48:51], v[52:55], v[4:19]
	ds_read_b64_tr_b16 v[52:53], v1 offset:35840
	ds_read_b64_tr_b16 v[54:55], v1 offset:36352
	s_waitcnt lgkmcnt(0)
	v_mfma_f32_32x32x16_bf16 v[4:19], v[36:39], v[52:55], v[4:19]
	ds_read_b64_tr_b16 v[52:53], v1 offset:36864
	ds_read_b64_tr_b16 v[54:55], v1 offset:37376
	s_waitcnt lgkmcnt(0)
	v_mfma_f32_32x32x16_bf16 v[20:35], v[40:43], v[52:55], v[20:35]
	ds_read_b64_tr_b16 v[40:41], v1 offset:37888
	ds_read_b64_tr_b16 v[42:43], v1 offset:38400
	s_waitcnt lgkmcnt(0)
	v_mfma_f32_32x32x16_bf16 v[20:35], v[44:47], v[40:43], v[20:35]
	ds_read_b64_tr_b16 v[40:41], v1 offset:38912
	ds_read_b64_tr_b16 v[42:43], v1 offset:39424
	s_waitcnt lgkmcnt(0)
	v_mfma_f32_32x32x16_bf16 v[20:35], v[48:51], v[40:43], v[20:35]
	ds_read_b64_tr_b16 v[40:41], v1 offset:39936
	ds_read_b64_tr_b16 v[42:43], v1 offset:40448
	s_waitcnt lgkmcnt(0)
	v_mfma_f32_32x32x16_bf16 v[20:35], v[36:39], v[40:43], v[20:35]

; #define LAS __attribute__((address_space(3)))
; __device__ __forceinline__ unsigned cvtpk(float lo, float hi) { typedef __bf16 bf16x2_t __attribute__((ext_vector_type(2))); f32x2 v = {lo, hi}; bf16x2_t b = __builtin_convertvector(v, bf16x2_t); return __builtin_bit_cast(unsigned, b); }
; __device__ __forceinline__ s16x4 vtr(const LAS unsigned char* p) { return __builtin_bit_cast(s16x4, __builtin_amdgcn_ds_read_tr16_b64_v4i16((LAS v4i16_t*)p)); }
; template <int D, bool MASK, bool BIAS, bool SINK, bool REV, bool O8, class BG>
; __device__ __forceinline__ void attn_unit(const Prm& P, LAS unsigned char* lds, BG& bg) {
;     ...
;             float sacc = 0.f;
; #pragma unroll
;             for (int r = 0; r < 16; ++r) { p0[r] = __builtin_amdgcn_exp2f(p0[r]); p1[r] = __builtin_amdgcn_exp2f(p1[r]); sacc += p0[r] + p1[r]; }
;             l_reg += sacc;
;             u32x4 pw[4];
; #pragma unroll
;             for (int q = 0; q < 4; ++q) { pw[0][q] = cvtpk(p0[2 * q], p0[2 * q + 1]); pw[1][q] = cvtpk(p0[8 + 2 * q], p0[9 + 2 * q]); pw[2][q] = cvtpk(p1[2 * q], p1[2 * q + 1]); pw[3][q] = cvtpk(p1[8 + 2 * q], p1[9 + 2 * q]); }
;             const LAS unsigned char* vs = lds + VOFF + s * KSLOT + ((lane >> 4) & 1) * 32 + (lane & 3) * 8 + (4 * hi + ((lane & 15) >> 2)) * 64;
; #pragma unroll
;             for (int d = 0; d < NDB; ++d)
; #pragma unroll
;                 for (int k4 = 0; k4 < 4; ++k4) {
;                     const s16x4 vlo = vtr(vs + d * 4096 + k4 * 1024), vhi = vtr(vs + d * 4096 + k4 * 1024 + 512);
;                     const bf16x8 vf = (bf16x8){vlo[0], vlo[1], vlo[2], vlo[3], vhi[0], vhi[1], vhi[2], vhi[3]};
;                     o[d] = __builtin_amdgcn_mfma_f32_32x32x16_bf16(__builtin_bit_cast(bf16x8, pw[k4]), vf, o[d], 0, 0, 0);
;                 }
.LBB0_610:
	v_exp_f32_e32 v91, v50
	v_exp_f32_e32 v200, v34
	v_exp_f32_e32 v82, v51
	v_exp_f32_e32 v192, v35
	v_exp_f32_e32 v201, v36
	v_add_f32_e32 v193, v200, v91
	v_exp_f32_e32 v194, v37
	v_pk_add_f32 v[34:35], v[192:193], v[82:83]
	v_exp_f32_e32 v193, v52
	v_pk_add_f32 v[50:51], v[34:35], v[34:35] op_sel_hi:[0,1]
	v_exp_f32_e32 v50, v53
	v_exp_f32_e32 v202, v42
	v_add_f32_e32 v195, v201, v193
	v_pk_add_f32 v[34:35], v[194:195], v[50:51]
	s_nop 0
	v_pk_add_f32 v[36:37], v[34:35], v[34:35] op_sel_hi:[0,1]
	v_exp_f32_e32 v51, v54
	v_exp_f32_e32 v195, v38
	v_exp_f32_e32 v36, v55
	v_exp_f32_e32 v54, v39
	v_add_f32_e32 v55, v195, v51
	v_pk_add_f32 v[34:35], v[54:55], v[36:37]
	s_nop 0
	v_pk_add_f32 v[38:39], v[34:35], v[34:35] op_sel_hi:[0,1]
	v_exp_f32_e32 v37, v56
	v_exp_f32_e32 v55, v40
	v_exp_f32_e32 v38, v57
	v_exp_f32_e32 v56, v41
	v_cvt_pk_bf16_f32 v36, v51, v36
	v_add_f32_e32 v57, v55, v37
	v_cvt_pk_bf16_f32 v37, v37, v38
	v_pk_add_f32 v[34:35], v[56:57], v[38:39]
	v_exp_f32_e32 v57, v58
	v_pk_add_f32 v[52:53], v[34:35], v[34:35] op_sel_hi:[0,1]
	v_exp_f32_e32 v52, v59
	v_exp_f32_e32 v58, v43
	v_add_f32_e32 v59, v202, v57
	v_exp_f32_e32 v43, v60
	v_exp_f32_e32 v60, v45
	v_pk_add_f32 v[34:35], v[58:59], v[52:53]
	v_exp_f32_e32 v59, v44
	v_pk_add_f32 v[196:197], v[34:35], v[34:35] op_sel_hi:[0,1]
	v_exp_f32_e32 v196, v61
	v_cvt_pk_bf16_f32 v42, v57, v52
	v_add_f32_e32 v61, v59, v43
	v_pk_add_f32 v[34:35], v[60:61], v[196:197]
	s_nop 0
	v_pk_add_f32 v[44:45], v[34:35], v[34:35] op_sel_hi:[0,1]
	v_exp_f32_e32 v61, v62
	v_exp_f32_e32 v197, v46
	v_exp_f32_e32 v44, v63
	v_exp_f32_e32 v62, v47
	v_cvt_pk_bf16_f32 v43, v43, v196
	v_add_f32_e32 v63, v197, v61
	v_cvt_pk_bf16_f32 v46, v202, v58
	v_pk_add_f32 v[34:35], v[62:63], v[44:45]
	v_exp_f32_e32 v63, v64
	v_pk_add_f32 v[198:199], v[34:35], v[34:35] op_sel_hi:[0,1]
	v_cvt_pk_bf16_f32 v34, v91, v82
	v_add_u32_e32 v82, s14, v162
	v_cvt_pk_bf16_f32 v35, v193, v50
	s_nop 0
	ds_read_b64_tr_b16 v[38:39], v82 offset:32768
	ds_read_b64_tr_b16 v[40:41], v82 offset:33280
	v_exp_f32_e32 v198, v65
	s_waitcnt lgkmcnt(0)
	v_mfma_f32_32x32x16_bf16 v[2:17], v[34:37], v[38:41], v[2:17]
	ds_read_b64_tr_b16 v[50:51], v82 offset:33792
	ds_read_b64_tr_b16 v[52:53], v82 offset:34304
	v_cvt_pk_bf16_f32 v44, v61, v44
	v_cvt_pk_bf16_f32 v45, v63, v198
	v_cvt_pk_bf16_f32 v38, v200, v192
	v_cvt_pk_bf16_f32 v39, v201, v194
	v_cvt_pk_bf16_f32 v40, v195, v54
	v_cvt_pk_bf16_f32 v41, v55, v56
	s_waitcnt lgkmcnt(0)
	v_mfma_f32_32x32x16_bf16 v[2:17], v[42:45], v[50:53], v[2:17]
	ds_read_b64_tr_b16 v[50:51], v82 offset:34816
	ds_read_b64_tr_b16 v[52:53], v82 offset:35328
	v_exp_f32_e32 v61, v48
	v_exp_f32_e32 v64, v49
	ds_read_b64_tr_b16 v[54:55], v82 offset:35840
	ds_read_b64_tr_b16 v[56:57], v82 offset:36352
	v_cvt_pk_bf16_f32 v47, v59, v60
	v_cvt_pk_bf16_f32 v48, v197, v62
	v_cvt_pk_bf16_f32 v49, v61, v64
	s_waitcnt lgkmcnt(2)
	v_mfma_f32_32x32x16_bf16 v[2:17], v[38:41], v[50:53], v[2:17]
	v_add_f32_e32 v65, v61, v63
	s_waitcnt lgkmcnt(0)
	v_mfma_f32_32x32x16_bf16 v[2:17], v[46:49], v[54:57], v[2:17]
	ds_read_b64_tr_b16 v[50:51], v82 offset:36864
	ds_read_b64_tr_b16 v[52:53], v82 offset:37376
	ds_read_b64_tr_b16 v[54:55], v82 offset:37888
	ds_read_b64_tr_b16 v[56:57], v82 offset:38400
	s_waitcnt lgkmcnt(2)
	v_mfma_f32_32x32x16_bf16 v[18:33], v[34:37], v[50:53], v[18:33]
	s_waitcnt lgkmcnt(0)
	v_mfma_f32_32x32x16_bf16 v[18:33], v[42:45], v[54:57], v[18:33]
	ds_read_b64_tr_b16 v[34:35], v82 offset:38912
	ds_read_b64_tr_b16 v[36:37], v82 offset:39424
	ds_read_b64_tr_b16 v[42:43], v82 offset:39936
	ds_read_b64_tr_b16 v[44:45], v82 offset:40448
	s_waitcnt lgkmcnt(2)
	v_mfma_f32_32x32x16_bf16 v[18:33], v[38:41], v[34:37], v[18:33]
	v_add_f32_e64 v34, v64, v198
	v_add_f32_e64 v35, v65, v199
	v_add_f32_e32 v34, v34, v35
	v_add_f32_e32 v87, v87, v34
	s_waitcnt lgkmcnt(0)
	v_mfma_f32_32x32x16_bf16 v[18:33], v[46:49], v[42:45], v[18:33]

; #define PG8_STAGE(bufoff, gbase, voff) do { _Pragma("unroll") for (int _i = 0; _i < 2; ++_i) \
;         __builtin_amdgcn_global_load_lds((const unsigned*)((const char*)(gbase) + (voff)[_i]), (LAS unsigned*)(lds + (bufoff) + ldsw + _i * 8192), 16, 0, 0); } while (0)
; #define PG8_LDA(dst, b, h) do { if constexpr (FP8) { _Pragma("unroll") for (int m = 0; m < 4; ++m) dst##8[m] = PG8_LD8(lds + PG8_SA(b, h) + aoff + m * 2048); } \
;         else { _Pragma("unroll") for (int m = 0; m < 4; ++m) _Pragma("unroll") for (int k = 0; k < 2; ++k) dst[m][k] = *(const LAS bf16x8*)(lds + PG8_SA(b, h) + aoff + m * 2048 + k * 1024); } } while (0)
; #define PG8_LDB(dst, b, h) do { if constexpr (FP8) { _Pragma("unroll") for (int n = 0; n < 2; ++n) dst##8[n] = PG8_LD8(lds + PG8_SB(b, h) + boff + n * 2048); } \
;         else { _Pragma("unroll") for (int n = 0; n < 2; ++n) _Pragma("unroll") for (int k = 0; k < 2; ++k) dst[n][k] = *(const LAS bf16x8*)(lds + PG8_SB(b, h) + boff + n * 2048 + k * 1024); } } while (0)
; #define PG8_WAIT_V(n) asm volatile("s_waitcnt vmcnt(" #n ")" ::: "memory")
; #define PG8_WAIT_L(n) asm volatile("s_waitcnt lgkmcnt(" #n ")" ::: "memory")
; template <class Epi, class Sched, bool ALIGN_EPI, bool SP2, bool FP8 = false>
; __device__ __forceinline__ void gemm_phase(LAS unsigned char* lds, const int K, const Sched& S, const Epi& E) {
;     ...
;         for (int t = 0; t < nt; t += 2) {
;             const bool last = (t == nt - 2);
;             const char* a1 = cA + (size_t)(t + 1) * kstep;
;             const char* a2 = last ? nA : cA + (size_t)(t + 2) * kstep; const char* b2 = last ? nB : cB + (size_t)(t + 2) * kstep;
;             const char* a3 = a2 + kstep; const char* b3 = b2 + kstep;
;             unsigned vX0[2], vX1[2];
; #pragma unroll
;             for (int i = 0; i < 2; ++i) { vX0[i] = last ? vAn[0][i] : vAc[0][i]; vX1[i] = last ? vAn[1][i] : vAc[1][i]; }
;             PG8_LDB(B0, 0, 0); PG8_LDB(B1, 0, 1); PG8_SCHED; PG8_LDA(At, 0, 0); PG8_STAGE(PG8_SA(1, 1), a1, vAc[1]);
;             PG8_WAIT_V(8); PG8_WAIT_L(0); PG8_BAR; PG8_MMA(0, 0, At, B0); PG8_MMA(0, 1, At, B1); PG8_BAR; PG8_SCHED;
;             PG8_LDA(At, 0, 1); PG8_STAGE(PG8_SB(0, 0), b2, voffB); PG8_STAGE(PG8_SB(0, 1), b2 + hstep, voffB); PG8_STAGE(PG8_SA(0, 0), a2, vX0);
;             PG8_WAIT_V(8); PG8_WAIT_L(0); PG8_BAR; PG8_MMA(1, 0, At, B0); PG8_MMA(1, 1, At, B1); PG8_BAR; PG8_SCHED;
.LBB0_790:
	ds_read_b128 v[18:21], v191
	ds_read_b128 v[22:25], v191 offset:1024
	ds_read_b128 v[26:29], v191 offset:2048
	ds_read_b128 v[30:33], v191 offset:3072
	ds_read_b128 v[2:5], v192
	ds_read_b128 v[6:9], v192 offset:1024
	ds_read_b128 v[10:13], v192 offset:2048
	ds_read_b128 v[14:17], v192 offset:3072
	s_add_u32 s60, s30, s58
	s_addc_u32 s61, s31, s59
	s_add_u32 s62, s60, 0x12000100
	s_addc_u32 s63, s61, 0
	s_add_u32 s72, s49, s58
	s_addc_u32 s73, s57, s59
	s_cmpk_eq_i32 s58, 0x700
	s_cselect_b64 vcc, -1, 0
	s_and_b64 s[60:61], vcc, exec
	v_cndmask_b32_e32 v166, v173, v195, vcc
	s_cselect_b32 s63, s9, s63
	s_cselect_b32 s62, s8, s62
	v_cndmask_b32_e32 v169, v168, v196, vcc
	v_cndmask_b32_e32 v232, v172, v197, vcc
	v_cndmask_b32_e32 v171, v170, v198, vcc
	s_cselect_b32 s61, s51, s73
	s_cselect_b32 s60, s50, s72
	v_lshl_add_u64 v[224:225], v[176:177], 0, s[58:59]
	s_add_i32 m0, s47, 0xc000
	ds_read_b128 v[178:181], v193
	ds_read_b128 v[182:185], v193 offset:1024
	ds_read_b128 v[200:203], v193 offset:2048
	ds_read_b128 v[204:207], v193 offset:3072
	ds_read_b128 v[208:211], v193 offset:4096
	ds_read_b128 v[212:215], v193 offset:5120
	ds_read_b128 v[216:219], v193 offset:6144
	ds_read_b128 v[220:223], v193 offset:7168
	global_load_lds_dwordx4 v[224:225], off
	v_lshl_add_u64 v[224:225], v[174:175], 0, s[58:59]
	s_add_i32 m0, s47, 0xe000
	s_nop 0
	global_load_lds_dwordx4 v[224:225], off
	s_waitcnt vmcnt(8)
	s_waitcnt lgkmcnt(0)
	s_setprio 1
	s_barrier
	v_mfma_f32_16x16x128_f8f6f4 v[158:161], v[18:25], v[178:185], v[158:161]
	v_mfma_f32_16x16x128_f8f6f4 v[154:157], v[26:33], v[178:185], v[154:157]
	v_mfma_f32_16x16x128_f8f6f4 v[142:145], v[18:25], v[200:207], v[142:145]
	v_mfma_f32_16x16x128_f8f6f4 v[138:141], v[26:33], v[200:207], v[138:141]
	v_mfma_f32_16x16x128_f8f6f4 v[126:129], v[18:25], v[208:215], v[126:129]
	v_mfma_f32_16x16x128_f8f6f4 v[122:125], v[26:33], v[208:215], v[122:125]
	v_mfma_f32_16x16x128_f8f6f4 v[110:113], v[18:25], v[216:223], v[110:113]
	v_mfma_f32_16x16x128_f8f6f4 v[106:109], v[26:33], v[216:223], v[106:109]
	v_mfma_f32_16x16x128_f8f6f4 v[150:153], v[2:9], v[178:185], v[150:153]
	v_mfma_f32_16x16x128_f8f6f4 v[146:149], v[10:17], v[178:185], v[146:149]
	v_mfma_f32_16x16x128_f8f6f4 v[134:137], v[2:9], v[200:207], v[134:137]
	v_mfma_f32_16x16x128_f8f6f4 v[130:133], v[10:17], v[200:207], v[130:133]
	v_mfma_f32_16x16x128_f8f6f4 v[118:121], v[2:9], v[208:215], v[118:121]
	v_mfma_f32_16x16x128_f8f6f4 v[114:117], v[10:17], v[208:215], v[114:117]
	v_mfma_f32_16x16x128_f8f6f4 v[102:105], v[2:9], v[216:223], v[102:105]
	v_mfma_f32_16x16x128_f8f6f4 v[98:101], v[10:17], v[216:223], v[98:101]
	s_setprio 0
	s_barrier
	s_add_i32 s72, s67, s35
	v_lshl_add_u64 v[178:179], s[60:61], 0, v[162:163]
	s_mov_b32 m0, s72
	ds_read_b128 v[200:203], v193 offset:16384
	ds_read_b128 v[204:207], v193 offset:17408
	ds_read_b128 v[208:211], v193 offset:18432
	ds_read_b128 v[212:215], v193 offset:19456
	ds_read_b128 v[216:219], v193 offset:20480
	ds_read_b128 v[220:223], v193 offset:21504
	ds_read_b128 v[224:227], v193 offset:22528
	ds_read_b128 v[228:231], v193 offset:23552
	global_load_lds_dwordx4 v[178:179], off
	s_add_i32 m0, s72, 0x2000
	s_add_u32 s72, s60, 0x40000
	v_lshl_add_u64 v[180:181], s[60:61], 0, v[164:165]
	s_addc_u32 s73, s61, 0
	s_add_i32 s74, s68, s35
	global_load_lds_dwordx4 v[180:181], off
	v_lshl_add_u64 v[182:183], s[72:73], 0, v[162:163]
	s_mov_b32 m0, s74
	v_mov_b32_e32 v233, v167
	global_load_lds_dwordx4 v[182:183], off
	v_lshl_add_u64 v[182:183], s[72:73], 0, v[164:165]
	s_add_i32 m0, s74, 0x2000
	v_lshl_add_u64 v[184:185], s[62:63], 0, v[166:167]
	global_load_lds_dwordx4 v[182:183], off
	s_mov_b32 m0, s47
	v_lshl_add_u64 v[182:183], s[62:63], 0, v[232:233]
	global_load_lds_dwordx4 v166, s[62:63]
	s_mov_b32 m0, s53
	s_nop 0
	global_load_lds_dwordx4 v232, s[62:63]
	s_waitcnt vmcnt(8)
	s_waitcnt lgkmcnt(0)
	s_setprio 1
	s_barrier
	v_mfma_f32_16x16x128_f8f6f4 v[94:97], v[18:25], v[200:207], v[94:97]
	v_mfma_f32_16x16x128_f8f6f4 v[90:93], v[26:33], v[200:207], v[90:93]
	v_mfma_f32_16x16x128_f8f6f4 v[78:81], v[18:25], v[208:215], v[78:81]
	v_mfma_f32_16x16x128_f8f6f4 v[74:77], v[26:33], v[208:215], v[74:77]
	v_mfma_f32_16x16x128_f8f6f4 v[54:57], v[18:25], v[216:223], v[54:57]
	v_mfma_f32_16x16x128_f8f6f4 v[50:53], v[26:33], v[216:223], v[50:53]
	v_mfma_f32_16x16x128_f8f6f4 v[38:41], v[18:25], v[224:231], v[38:41]
	v_mfma_f32_16x16x128_f8f6f4 v[34:37], v[26:33], v[224:231], v[34:37]
	v_mfma_f32_16x16x128_f8f6f4 v[86:89], v[2:9], v[200:207], v[86:89]
	v_mfma_f32_16x16x128_f8f6f4 v[82:85], v[10:17], v[200:207], v[82:85]
	v_mfma_f32_16x16x128_f8f6f4 v[70:73], v[2:9], v[208:215], v[70:73]
	v_mfma_f32_16x16x128_f8f6f4 v[66:69], v[10:17], v[208:215], v[66:69]
	v_mfma_f32_16x16x128_f8f6f4 v[62:65], v[2:9], v[216:223], v[62:65]
	v_mfma_f32_16x16x128_f8f6f4 v[58:61], v[10:17], v[216:223], v[58:61]
	v_mfma_f32_16x16x128_f8f6f4 v[46:49], v[2:9], v[224:231], v[46:49]
	v_mfma_f32_16x16x128_f8f6f4 v[42:45], v[10:17], v[224:231], v[42:45]
	s_setprio 0
	s_barrier
; #define PG8_STAGE(bufoff, gbase, voff) do { _Pragma("unroll") for (int _i = 0; _i < 2; ++_i) \
;         __builtin_amdgcn_global_load_lds((const unsigned*)((const char*)(gbase) + (voff)[_i]), (LAS unsigned*)(lds + (bufoff) + ldsw + _i * 8192), 16, 0, 0); } while (0)
; #define PG8_LDA(dst, b, h) do { if constexpr (FP8) { _Pragma("unroll") for (int m = 0; m < 4; ++m) dst##8[m] = PG8_LD8(lds + PG8_SA(b, h) + aoff + m * 2048); } \
;         else { _Pragma("unroll") for (int m = 0; m < 4; ++m) _Pragma("unroll") for (int k = 0; k < 2; ++k) dst[m][k] = *(const LAS bf16x8*)(lds + PG8_SA(b, h) + aoff + m * 2048 + k * 1024); } } while (0)
; #define PG8_LDB(dst, b, h) do { if constexpr (FP8) { _Pragma("unroll") for (int n = 0; n < 2; ++n) dst##8[n] = PG8_LD8(lds + PG8_SB(b, h) + boff + n * 2048); } \
;         else { _Pragma("unroll") for (int n = 0; n < 2; ++n) _Pragma("unroll") for (int k = 0; k < 2; ++k) dst[n][k] = *(const LAS bf16x8*)(lds + PG8_SB(b, h) + boff + n * 2048 + k * 1024); } } while (0)
; #define PG8_WAIT_V(n) asm volatile("s_waitcnt vmcnt(" #n ")" ::: "memory")
; #define PG8_WAIT_L(n) asm volatile("s_waitcnt lgkmcnt(" #n ")" ::: "memory")
; #define PG8_BAR __builtin_amdgcn_s_barrier()
; #define PG8_SCHED __builtin_amdgcn_sched_barrier(0)
; template <class Epi, class Sched, bool ALIGN_EPI, bool SP2, bool FP8 = false>
; __device__ __forceinline__ void gemm_phase(LAS unsigned char* lds, const int K, const Sched& S, const Epi& E) {
;     ...
;             PG8_LDB(B0, 1, 0); PG8_LDB(B1, 1, 1); PG8_SCHED; PG8_LDA(At, 1, 0); PG8_STAGE(PG8_SA(0, 1), a2, vX1);
;             PG8_WAIT_V(8); PG8_WAIT_L(0); PG8_BAR; PG8_MMA(0, 0, At, B0); PG8_MMA(0, 1, At, B1); PG8_BAR; PG8_SCHED;
;             PG8_LDA(At, 1, 1); PG8_STAGE(PG8_SB(1, 0), b3, voffB); PG8_STAGE(PG8_SB(1, 1), b3 + hstep, voffB); PG8_STAGE(PG8_SA(1, 0), a3, vX0);
;             PG8_WAIT_V(8); PG8_WAIT_L(0); PG8_BAR; PG8_MMA(1, 0, At, B0); PG8_MMA(1, 1, At, B1); PG8_BAR; PG8_SCHED;
;         }
;         if constexpr (ALIGN_EPI) { if (wr == 0) PG8_BAR; }
	s_add_i32 s72, 0, 0x18000
	s_add_i32 s73, 0, 0x1c000
	v_add_u32_e32 v14, s72, v188
	v_add_u32_e32 v30, s73, v188
	ds_read_b128 v[2:5], v14
	ds_read_b128 v[6:9], v14 offset:1024
	ds_read_b128 v[10:13], v14 offset:2048
	ds_read_b128 v[14:17], v14 offset:3072
	ds_read_b128 v[18:21], v30
	ds_read_b128 v[22:25], v30 offset:1024
	ds_read_b128 v[26:29], v30 offset:2048
	ds_read_b128 v[30:33], v30 offset:3072
	s_mov_b32 m0, s54
	ds_read_b128 v[200:203], v193 offset:32768
	ds_read_b128 v[204:207], v193 offset:33792
	ds_read_b128 v[208:211], v193 offset:34816
	ds_read_b128 v[212:215], v193 offset:35840
	ds_read_b128 v[216:219], v193 offset:36864
	ds_read_b128 v[220:223], v193 offset:37888
	ds_read_b128 v[224:227], v193 offset:38912
	ds_read_b128 v[228:231], v193 offset:39936
	global_load_lds_dwordx4 v169, s[62:63]
	s_mov_b32 m0, s55
	s_nop 0
	global_load_lds_dwordx4 v171, s[62:63]
	s_waitcnt vmcnt(8)
	s_waitcnt lgkmcnt(0)
	s_setprio 1
	s_barrier
	v_mfma_f32_16x16x128_f8f6f4 v[158:161], v[2:9], v[200:207], v[158:161]
	v_mfma_f32_16x16x128_f8f6f4 v[154:157], v[10:17], v[200:207], v[154:157]
	v_mfma_f32_16x16x128_f8f6f4 v[142:145], v[2:9], v[208:215], v[142:145]
	v_mfma_f32_16x16x128_f8f6f4 v[138:141], v[10:17], v[208:215], v[138:141]
	v_mfma_f32_16x16x128_f8f6f4 v[126:129], v[2:9], v[216:223], v[126:129]
	v_mfma_f32_16x16x128_f8f6f4 v[122:125], v[10:17], v[216:223], v[122:125]
	v_mfma_f32_16x16x128_f8f6f4 v[110:113], v[2:9], v[224:231], v[110:113]
	v_mfma_f32_16x16x128_f8f6f4 v[106:109], v[10:17], v[224:231], v[106:109]
	v_mfma_f32_16x16x128_f8f6f4 v[150:153], v[18:25], v[200:207], v[150:153]
	v_mfma_f32_16x16x128_f8f6f4 v[146:149], v[26:33], v[200:207], v[146:149]
	v_mfma_f32_16x16x128_f8f6f4 v[134:137], v[18:25], v[208:215], v[134:137]
	v_mfma_f32_16x16x128_f8f6f4 v[130:133], v[26:33], v[208:215], v[130:133]
	v_mfma_f32_16x16x128_f8f6f4 v[118:121], v[18:25], v[216:223], v[118:121]
	v_mfma_f32_16x16x128_f8f6f4 v[114:117], v[26:33], v[216:223], v[114:117]
	v_mfma_f32_16x16x128_f8f6f4 v[102:105], v[18:25], v[224:231], v[102:105]
	v_mfma_f32_16x16x128_f8f6f4 v[98:101], v[26:33], v[224:231], v[98:101]
	s_setprio 0
	s_barrier
	s_add_i32 s62, s72, s35
	v_lshl_add_u64 v[178:179], v[178:179], 0, s[40:41]
	s_mov_b32 m0, s62
	ds_read_b128 v[200:203], v193 offset:49152
	ds_read_b128 v[204:207], v193 offset:50176
	ds_read_b128 v[208:211], v193 offset:51200
	ds_read_b128 v[212:215], v193 offset:52224
	ds_read_b128 v[216:219], v193 offset:53248
	ds_read_b128 v[220:223], v193 offset:54272
	ds_read_b128 v[224:227], v193 offset:55296
	ds_read_b128 v[228:231], v193 offset:56320
	global_load_lds_dwordx4 v[178:179], off
	s_add_i32 m0, s62, 0x2000
	s_add_u32 s60, s60, 0x40080
	v_lshl_add_u64 v[178:179], v[180:181], 0, s[40:41]
	s_addc_u32 s61, s61, 0
	s_add_i32 s62, s73, s35
	global_load_lds_dwordx4 v[178:179], off
	v_lshl_add_u64 v[178:179], s[60:61], 0, v[162:163]
	s_mov_b32 m0, s62
	s_nop 0
	global_load_lds_dwordx4 v[178:179], off
	v_lshl_add_u64 v[178:179], s[60:61], 0, v[164:165]
	s_add_i32 m0, s62, 0x2000
	s_nop 0
	global_load_lds_dwordx4 v[178:179], off
	v_lshl_add_u64 v[178:179], v[184:185], 0, s[40:41]
	s_mov_b32 m0, s65
	s_nop 0
	global_load_lds_dwordx4 v[178:179], off
	v_lshl_add_u64 v[178:179], v[182:183], 0, s[40:41]
	s_mov_b32 m0, s66
	s_nop 0
	global_load_lds_dwordx4 v[178:179], off
	s_waitcnt vmcnt(8)
	s_waitcnt lgkmcnt(0)
	s_setprio 1
	s_barrier
	v_mfma_f32_16x16x128_f8f6f4 v[94:97], v[2:9], v[200:207], v[94:97]
	v_mfma_f32_16x16x128_f8f6f4 v[90:93], v[10:17], v[200:207], v[90:93]
	v_mfma_f32_16x16x128_f8f6f4 v[78:81], v[2:9], v[208:215], v[78:81]
	v_mfma_f32_16x16x128_f8f6f4 v[74:77], v[10:17], v[208:215], v[74:77]
	v_mfma_f32_16x16x128_f8f6f4 v[54:57], v[2:9], v[216:223], v[54:57]
	v_mfma_f32_16x16x128_f8f6f4 v[50:53], v[10:17], v[216:223], v[50:53]
	v_mfma_f32_16x16x128_f8f6f4 v[38:41], v[2:9], v[224:231], v[38:41]
	v_mfma_f32_16x16x128_f8f6f4 v[34:37], v[10:17], v[224:231], v[34:37]
	v_mfma_f32_16x16x128_f8f6f4 v[86:89], v[18:25], v[200:207], v[86:89]
	v_mfma_f32_16x16x128_f8f6f4 v[82:85], v[26:33], v[200:207], v[82:85]
	v_mfma_f32_16x16x128_f8f6f4 v[70:73], v[18:25], v[208:215], v[70:73]
	v_mfma_f32_16x16x128_f8f6f4 v[66:69], v[26:33], v[208:215], v[66:69]
	v_mfma_f32_16x16x128_f8f6f4 v[62:65], v[18:25], v[216:223], v[62:65]
	v_mfma_f32_16x16x128_f8f6f4 v[58:61], v[26:33], v[216:223], v[58:61]
	v_mfma_f32_16x16x128_f8f6f4 v[46:49], v[18:25], v[224:231], v[46:49]
	v_mfma_f32_16x16x128_f8f6f4 v[42:45], v[26:33], v[224:231], v[42:45]
	s_setprio 0
	s_barrier
	s_add_i32 s71, s71, 2
	s_add_u32 s58, s58, 0x100
	s_addc_u32 s59, s59, 0
	s_cmp_gt_u32 s71, 13
	s_cbranch_scc0 .LBB0_790
	s_and_b64 vcc, exec, s[44:45]
	s_cbranch_vccz .LBB0_793
	s_barrier

; #define PG8_STAGE(bufoff, gbase, voff) do { _Pragma("unroll") for (int _i = 0; _i < 2; ++_i) \
;         __builtin_amdgcn_global_load_lds((const unsigned*)((const char*)(gbase) + (voff)[_i]), (LAS unsigned*)(lds + (bufoff) + ldsw + _i * 8192), 16, 0, 0); } while (0)
; #define PG8_LDA(dst, b, h) do { if constexpr (FP8) { _Pragma("unroll") for (int m = 0; m < 4; ++m) dst##8[m] = PG8_LD8(lds + PG8_SA(b, h) + aoff + m * 2048); } \
;         else { _Pragma("unroll") for (int m = 0; m < 4; ++m) _Pragma("unroll") for (int k = 0; k < 2; ++k) dst[m][k] = *(const LAS bf16x8*)(lds + PG8_SA(b, h) + aoff + m * 2048 + k * 1024); } } while (0)
; #define PG8_LDB(dst, b, h) do { if constexpr (FP8) { _Pragma("unroll") for (int n = 0; n < 2; ++n) dst##8[n] = PG8_LD8(lds + PG8_SB(b, h) + boff + n * 2048); } \
;         else { _Pragma("unroll") for (int n = 0; n < 2; ++n) _Pragma("unroll") for (int k = 0; k < 2; ++k) dst[n][k] = *(const LAS bf16x8*)(lds + PG8_SB(b, h) + boff + n * 2048 + k * 1024); } } while (0)
; #define PG8_WAIT_V(n) asm volatile("s_waitcnt vmcnt(" #n ")" ::: "memory")
; #define PG8_WAIT_L(n) asm volatile("s_waitcnt lgkmcnt(" #n ")" ::: "memory")
; template <class Epi, class Sched, bool ALIGN_EPI, bool SP2, bool FP8 = false>
; __device__ __forceinline__ void gemm_phase(LAS unsigned char* lds, const int K, const Sched& S, const Epi& E) {
;     ...
;         for (int t = 0; t < nt; t += 2) {
;             const bool last = (t == nt - 2);
;             const char* a1 = cA + (size_t)(t + 1) * kstep;
;             const char* a2 = last ? nA : cA + (size_t)(t + 2) * kstep; const char* b2 = last ? nB : cB + (size_t)(t + 2) * kstep;
;             const char* a3 = a2 + kstep; const char* b3 = b2 + kstep;
;             unsigned vX0[2], vX1[2];
; #pragma unroll
;             for (int i = 0; i < 2; ++i) { vX0[i] = last ? vAn[0][i] : vAc[0][i]; vX1[i] = last ? vAn[1][i] : vAc[1][i]; }
;             PG8_LDB(B0, 0, 0); PG8_LDB(B1, 0, 1); PG8_SCHED; PG8_LDA(At, 0, 0); PG8_STAGE(PG8_SA(1, 1), a1, vAc[1]);
;             PG8_WAIT_V(8); PG8_WAIT_L(0); PG8_BAR; PG8_MMA(0, 0, At, B0); PG8_MMA(0, 1, At, B1); PG8_BAR; PG8_SCHED;
;             PG8_LDA(At, 0, 1); PG8_STAGE(PG8_SB(0, 0), b2, voffB); PG8_STAGE(PG8_SB(0, 1), b2 + hstep, voffB); PG8_STAGE(PG8_SA(0, 0), a2, vX0);
;             PG8_WAIT_V(8); PG8_WAIT_L(0); PG8_BAR; PG8_MMA(1, 0, At, B0); PG8_MMA(1, 1, At, B1); PG8_BAR; PG8_SCHED;
.LBB0_883:
	ds_read_b128 v[162:165], v153
	ds_read_b128 v[166:169], v153 offset:1024
	ds_read_b128 v[170:173], v153 offset:2048
	ds_read_b128 v[174:177], v153 offset:3072
	ds_read_b128 v[178:181], v154
	ds_read_b128 v[182:185], v154 offset:1024
	ds_read_b128 v[186:189], v154 offset:2048
	ds_read_b128 v[192:195], v154 offset:3072
	s_add_u32 s6, s30, s4
	s_addc_u32 s7, s31, s5
	s_add_u32 s50, s6, 0x1e000100
	s_addc_u32 s51, s7, 0
	s_add_u32 s70, s47, s4
	s_addc_u32 s71, s68, s5
	s_cmpk_eq_i32 s4, 0xf00
	s_cselect_b64 vcc, -1, 0
	s_and_b64 s[6:7], vcc, exec
	v_cndmask_b32_e32 v136, v143, v158, vcc
	s_cselect_b32 s51, s15, s51
	s_cselect_b32 s50, s14, s50
	v_cndmask_b32_e32 v139, v138, v159, vcc
	v_cndmask_b32_e32 v228, v142, v160, vcc
	v_cndmask_b32_e32 v141, v140, v161, vcc
	s_cselect_b32 s7, s49, s71
	s_cselect_b32 s6, s48, s70
	s_mov_b32 m0, s64
	v_lshl_add_u64 v[230:231], v[146:147], 0, s[4:5]
	ds_read_b128 v[196:199], v155
	ds_read_b128 v[200:203], v155 offset:1024
	ds_read_b128 v[204:207], v155 offset:2048
	ds_read_b128 v[208:211], v155 offset:3072
	ds_read_b128 v[212:215], v155 offset:4096
	ds_read_b128 v[216:219], v155 offset:5120
	ds_read_b128 v[220:223], v155 offset:6144
	ds_read_b128 v[224:227], v155 offset:7168
	global_load_lds_dwordx4 v[230:231], off
	v_lshl_add_u64 v[230:231], v[144:145], 0, s[4:5]
	s_add_i32 m0, s53, 0xe000
	s_nop 0
	global_load_lds_dwordx4 v[230:231], off
	s_waitcnt vmcnt(8)
	s_waitcnt lgkmcnt(0)
	s_setprio 1
	s_barrier
	v_mfma_f32_16x16x32_bf16 v[126:129], v[162:165], v[196:199], v[126:129]
	v_mfma_f32_16x16x32_bf16 v[122:125], v[170:173], v[196:199], v[122:125]
	v_mfma_f32_16x16x32_bf16 v[118:121], v[162:165], v[204:207], v[118:121]
	v_mfma_f32_16x16x32_bf16 v[114:117], v[170:173], v[204:207], v[114:117]
	v_mfma_f32_16x16x32_bf16 v[94:97], v[162:165], v[212:215], v[94:97]
	v_mfma_f32_16x16x32_bf16 v[90:93], v[170:173], v[212:215], v[90:93]
	v_mfma_f32_16x16x32_bf16 v[78:81], v[162:165], v[220:223], v[78:81]
	v_mfma_f32_16x16x32_bf16 v[74:77], v[170:173], v[220:223], v[74:77]
	v_mfma_f32_16x16x32_bf16 v[126:129], v[166:169], v[200:203], v[126:129]
	v_mfma_f32_16x16x32_bf16 v[122:125], v[174:177], v[200:203], v[122:125]
	v_mfma_f32_16x16x32_bf16 v[118:121], v[166:169], v[208:211], v[118:121]
	v_mfma_f32_16x16x32_bf16 v[114:117], v[174:177], v[208:211], v[114:117]
	v_mfma_f32_16x16x32_bf16 v[94:97], v[166:169], v[216:219], v[94:97]
	v_mfma_f32_16x16x32_bf16 v[90:93], v[174:177], v[216:219], v[90:93]
	v_mfma_f32_16x16x32_bf16 v[78:81], v[166:169], v[224:227], v[78:81]
	v_mfma_f32_16x16x32_bf16 v[74:77], v[174:177], v[224:227], v[74:77]
	v_mfma_f32_16x16x32_bf16 v[110:113], v[178:181], v[196:199], v[110:113]
	v_mfma_f32_16x16x32_bf16 v[106:109], v[186:189], v[196:199], v[106:109]
	v_mfma_f32_16x16x32_bf16 v[102:105], v[178:181], v[204:207], v[102:105]
	v_mfma_f32_16x16x32_bf16 v[98:101], v[186:189], v[204:207], v[98:101]
	v_mfma_f32_16x16x32_bf16 v[86:89], v[178:181], v[212:215], v[86:89]
	v_mfma_f32_16x16x32_bf16 v[82:85], v[186:189], v[212:215], v[82:85]
	v_mfma_f32_16x16x32_bf16 v[70:73], v[178:181], v[220:223], v[70:73]
	v_mfma_f32_16x16x32_bf16 v[66:69], v[186:189], v[220:223], v[66:69]
	v_mfma_f32_16x16x32_bf16 v[110:113], v[182:185], v[200:203], v[110:113]
	v_mfma_f32_16x16x32_bf16 v[106:109], v[192:195], v[200:203], v[106:109]
	v_mfma_f32_16x16x32_bf16 v[102:105], v[182:185], v[208:211], v[102:105]
	v_mfma_f32_16x16x32_bf16 v[98:101], v[192:195], v[208:211], v[98:101]
	v_mfma_f32_16x16x32_bf16 v[86:89], v[182:185], v[216:219], v[86:89]
	v_mfma_f32_16x16x32_bf16 v[82:85], v[192:195], v[216:219], v[82:85]
	v_mfma_f32_16x16x32_bf16 v[70:73], v[182:185], v[224:227], v[70:73]
	v_mfma_f32_16x16x32_bf16 v[66:69], v[192:195], v[224:227], v[66:69]
	s_setprio 0
	s_barrier
	s_add_i32 s70, s60, s35
	v_lshl_add_u64 v[230:231], s[6:7], 0, v[132:133]
	s_mov_b32 m0, s70
	ds_read_b128 v[196:199], v155 offset:16384
	ds_read_b128 v[200:203], v155 offset:17408
	ds_read_b128 v[204:207], v155 offset:18432
	ds_read_b128 v[208:211], v155 offset:19456
	ds_read_b128 v[212:215], v155 offset:20480
	ds_read_b128 v[216:219], v155 offset:21504
	ds_read_b128 v[220:223], v155 offset:22528
	ds_read_b128 v[224:227], v155 offset:23552
	global_load_lds_dwordx4 v[230:231], off
	s_add_i32 m0, s70, 0x2000
	s_add_u32 s70, s6, 0x80000
	v_lshl_add_u64 v[232:233], s[6:7], 0, v[134:135]
	s_addc_u32 s71, s7, 0
	s_add_i32 s72, s61, s35
	global_load_lds_dwordx4 v[232:233], off
	v_lshl_add_u64 v[234:235], s[70:71], 0, v[132:133]
	s_mov_b32 m0, s72
	v_mov_b32_e32 v229, v137
	global_load_lds_dwordx4 v[234:235], off
	v_lshl_add_u64 v[234:235], s[70:71], 0, v[134:135]
	s_add_i32 m0, s72, 0x2000
	s_nop 0
	global_load_lds_dwordx4 v[234:235], off
	s_mov_b32 m0, s53
	v_lshl_add_u64 v[234:235], s[50:51], 0, v[136:137]
	global_load_lds_dwordx4 v136, s[50:51]
	s_mov_b32 m0, s54
	s_nop 0
	global_load_lds_dwordx4 v228, s[50:51]
	s_waitcnt vmcnt(8)
	s_waitcnt lgkmcnt(0)
	v_lshl_add_u64 v[228:229], s[50:51], 0, v[228:229]
	s_setprio 1
	s_barrier
; #define PG8_STAGE(bufoff, gbase, voff) do { _Pragma("unroll") for (int _i = 0; _i < 2; ++_i) \
;         __builtin_amdgcn_global_load_lds((const unsigned*)((const char*)(gbase) + (voff)[_i]), (LAS unsigned*)(lds + (bufoff) + ldsw + _i * 8192), 16, 0, 0); } while (0)
; #define PG8_LDA(dst, b, h) do { if constexpr (FP8) { _Pragma("unroll") for (int m = 0; m < 4; ++m) dst##8[m] = PG8_LD8(lds + PG8_SA(b, h) + aoff + m * 2048); } \
;         else { _Pragma("unroll") for (int m = 0; m < 4; ++m) _Pragma("unroll") for (int k = 0; k < 2; ++k) dst[m][k] = *(const LAS bf16x8*)(lds + PG8_SA(b, h) + aoff + m * 2048 + k * 1024); } } while (0)
; #define PG8_LDB(dst, b, h) do { if constexpr (FP8) { _Pragma("unroll") for (int n = 0; n < 2; ++n) dst##8[n] = PG8_LD8(lds + PG8_SB(b, h) + boff + n * 2048); } \
;         else { _Pragma("unroll") for (int n = 0; n < 2; ++n) _Pragma("unroll") for (int k = 0; k < 2; ++k) dst[n][k] = *(const LAS bf16x8*)(lds + PG8_SB(b, h) + boff + n * 2048 + k * 1024); } } while (0)
; #define PG8_WAIT_V(n) asm volatile("s_waitcnt vmcnt(" #n ")" ::: "memory")
; #define PG8_WAIT_L(n) asm volatile("s_waitcnt lgkmcnt(" #n ")" ::: "memory")
; #define PG8_BAR __builtin_amdgcn_s_barrier()
; #define PG8_SCHED __builtin_amdgcn_sched_barrier(0)
; template <class Epi, class Sched, bool ALIGN_EPI, bool SP2, bool FP8 = false>
; __device__ __forceinline__ void gemm_phase(LAS unsigned char* lds, const int K, const Sched& S, const Epi& E) {
;     ...
;             PG8_WAIT_V(8); PG8_WAIT_L(0); PG8_BAR; PG8_MMA(1, 0, At, B0); PG8_MMA(1, 1, At, B1); PG8_BAR; PG8_SCHED;
;             PG8_LDB(B0, 1, 0); PG8_LDB(B1, 1, 1); PG8_SCHED; PG8_LDA(At, 1, 0); PG8_STAGE(PG8_SA(0, 1), a2, vX1);
;             PG8_WAIT_V(8); PG8_WAIT_L(0); PG8_BAR; PG8_MMA(0, 0, At, B0); PG8_MMA(0, 1, At, B1); PG8_BAR; PG8_SCHED;
	v_mfma_f32_16x16x32_bf16 v[62:65], v[162:165], v[196:199], v[62:65]
	v_mfma_f32_16x16x32_bf16 v[58:61], v[170:173], v[196:199], v[58:61]
	v_mfma_f32_16x16x32_bf16 v[46:49], v[162:165], v[204:207], v[46:49]
	v_mfma_f32_16x16x32_bf16 v[42:45], v[170:173], v[204:207], v[42:45]
	v_mfma_f32_16x16x32_bf16 v[22:25], v[162:165], v[212:215], v[22:25]
	v_mfma_f32_16x16x32_bf16 v[18:21], v[170:173], v[212:215], v[18:21]
	v_mfma_f32_16x16x32_bf16 v[6:9], v[162:165], v[220:223], v[6:9]
	v_mfma_f32_16x16x32_bf16 v[2:5], v[170:173], v[220:223], v[2:5]
	v_mfma_f32_16x16x32_bf16 v[62:65], v[166:169], v[200:203], v[62:65]
	v_mfma_f32_16x16x32_bf16 v[58:61], v[174:177], v[200:203], v[58:61]
	v_mfma_f32_16x16x32_bf16 v[46:49], v[166:169], v[208:211], v[46:49]
	v_mfma_f32_16x16x32_bf16 v[42:45], v[174:177], v[208:211], v[42:45]
	v_mfma_f32_16x16x32_bf16 v[22:25], v[166:169], v[216:219], v[22:25]
	v_mfma_f32_16x16x32_bf16 v[18:21], v[174:177], v[216:219], v[18:21]
	v_mfma_f32_16x16x32_bf16 v[6:9], v[166:169], v[224:227], v[6:9]
	v_mfma_f32_16x16x32_bf16 v[2:5], v[174:177], v[224:227], v[2:5]
	v_mfma_f32_16x16x32_bf16 v[54:57], v[178:181], v[196:199], v[54:57]
	v_mfma_f32_16x16x32_bf16 v[50:53], v[186:189], v[196:199], v[50:53]
	v_mfma_f32_16x16x32_bf16 v[30:33], v[178:181], v[204:207], v[30:33]
	v_mfma_f32_16x16x32_bf16 v[26:29], v[186:189], v[204:207], v[26:29]
	v_mfma_f32_16x16x32_bf16 v[34:37], v[178:181], v[212:215], v[34:37]
	v_mfma_f32_16x16x32_bf16 v[38:41], v[186:189], v[212:215], v[38:41]
	v_mfma_f32_16x16x32_bf16 v[10:13], v[178:181], v[220:223], v[10:13]
	v_mfma_f32_16x16x32_bf16 v[14:17], v[186:189], v[220:223], v[14:17]
	v_mfma_f32_16x16x32_bf16 v[54:57], v[182:185], v[200:203], v[54:57]
	v_mfma_f32_16x16x32_bf16 v[50:53], v[192:195], v[200:203], v[50:53]
	v_mfma_f32_16x16x32_bf16 v[30:33], v[182:185], v[208:211], v[30:33]
	v_mfma_f32_16x16x32_bf16 v[26:29], v[192:195], v[208:211], v[26:29]
	v_mfma_f32_16x16x32_bf16 v[34:37], v[182:185], v[216:219], v[34:37]
	v_mfma_f32_16x16x32_bf16 v[38:41], v[192:195], v[216:219], v[38:41]
	v_mfma_f32_16x16x32_bf16 v[10:13], v[182:185], v[224:227], v[10:13]
	v_mfma_f32_16x16x32_bf16 v[14:17], v[192:195], v[224:227], v[14:17]
	s_setprio 0
	s_barrier
	s_add_i32 s70, 0, 0x18000
	v_add_u32_e32 v136, s70, v151
	s_add_i32 s71, 0, 0x1c000
	ds_read_b128 v[162:165], v136
	ds_read_b128 v[166:169], v136 offset:1024
	ds_read_b128 v[170:173], v136 offset:2048
	ds_read_b128 v[174:177], v136 offset:3072
	v_add_u32_e32 v136, s71, v151
	ds_read_b128 v[178:181], v136
	ds_read_b128 v[182:185], v136 offset:1024
	ds_read_b128 v[186:189], v136 offset:2048
	ds_read_b128 v[192:195], v136 offset:3072
	s_mov_b32 m0, s55
	ds_read_b128 v[196:199], v155 offset:32768
	ds_read_b128 v[200:203], v155 offset:33792
	ds_read_b128 v[204:207], v155 offset:34816
	ds_read_b128 v[208:211], v155 offset:35840
	ds_read_b128 v[212:215], v155 offset:36864
	ds_read_b128 v[216:219], v155 offset:37888
	ds_read_b128 v[220:223], v155 offset:38912
	ds_read_b128 v[224:227], v155 offset:39936
	global_load_lds_dwordx4 v139, s[50:51]
	s_mov_b32 m0, s56
	s_nop 0
	global_load_lds_dwordx4 v141, s[50:51]
	s_waitcnt vmcnt(8)
	s_waitcnt lgkmcnt(0)
	s_setprio 1
	s_barrier
	v_mfma_f32_16x16x32_bf16 v[126:129], v[162:165], v[196:199], v[126:129]
	v_mfma_f32_16x16x32_bf16 v[122:125], v[170:173], v[196:199], v[122:125]
	v_mfma_f32_16x16x32_bf16 v[118:121], v[162:165], v[204:207], v[118:121]
	v_mfma_f32_16x16x32_bf16 v[114:117], v[170:173], v[204:207], v[114:117]
	v_mfma_f32_16x16x32_bf16 v[94:97], v[162:165], v[212:215], v[94:97]
	v_mfma_f32_16x16x32_bf16 v[90:93], v[170:173], v[212:215], v[90:93]
	v_mfma_f32_16x16x32_bf16 v[78:81], v[162:165], v[220:223], v[78:81]
	v_mfma_f32_16x16x32_bf16 v[74:77], v[170:173], v[220:223], v[74:77]
	v_mfma_f32_16x16x32_bf16 v[126:129], v[166:169], v[200:203], v[126:129]
	v_mfma_f32_16x16x32_bf16 v[122:125], v[174:177], v[200:203], v[122:125]
	v_mfma_f32_16x16x32_bf16 v[118:121], v[166:169], v[208:211], v[118:121]
	v_mfma_f32_16x16x32_bf16 v[114:117], v[174:177], v[208:211], v[114:117]
	v_mfma_f32_16x16x32_bf16 v[94:97], v[166:169], v[216:219], v[94:97]
	v_mfma_f32_16x16x32_bf16 v[90:93], v[174:177], v[216:219], v[90:93]
	v_mfma_f32_16x16x32_bf16 v[78:81], v[166:169], v[224:227], v[78:81]
	v_mfma_f32_16x16x32_bf16 v[74:77], v[174:177], v[224:227], v[74:77]
	v_mfma_f32_16x16x32_bf16 v[110:113], v[178:181], v[196:199], v[110:113]
	v_mfma_f32_16x16x32_bf16 v[106:109], v[186:189], v[196:199], v[106:109]
	v_mfma_f32_16x16x32_bf16 v[102:105], v[178:181], v[204:207], v[102:105]
	v_mfma_f32_16x16x32_bf16 v[98:101], v[186:189], v[204:207], v[98:101]
	v_mfma_f32_16x16x32_bf16 v[86:89], v[178:181], v[212:215], v[86:89]
	v_mfma_f32_16x16x32_bf16 v[82:85], v[186:189], v[212:215], v[82:85]
	v_mfma_f32_16x16x32_bf16 v[70:73], v[178:181], v[220:223], v[70:73]
	v_mfma_f32_16x16x32_bf16 v[66:69], v[186:189], v[220:223], v[66:69]
	v_mfma_f32_16x16x32_bf16 v[110:113], v[182:185], v[200:203], v[110:113]
	v_mfma_f32_16x16x32_bf16 v[106:109], v[192:195], v[200:203], v[106:109]
	v_mfma_f32_16x16x32_bf16 v[102:105], v[182:185], v[208:211], v[102:105]
	v_mfma_f32_16x16x32_bf16 v[98:101], v[192:195], v[208:211], v[98:101]
	v_mfma_f32_16x16x32_bf16 v[86:89], v[182:185], v[216:219], v[86:89]
	v_mfma_f32_16x16x32_bf16 v[82:85], v[192:195], v[216:219], v[82:85]
	v_mfma_f32_16x16x32_bf16 v[70:73], v[182:185], v[224:227], v[70:73]
	v_mfma_f32_16x16x32_bf16 v[66:69], v[192:195], v[224:227], v[66:69]
	s_setprio 0
	s_barrier
; #define PG8_STAGE(bufoff, gbase, voff) do { _Pragma("unroll") for (int _i = 0; _i < 2; ++_i) \
;         __builtin_amdgcn_global_load_lds((const unsigned*)((const char*)(gbase) + (voff)[_i]), (LAS unsigned*)(lds + (bufoff) + ldsw + _i * 8192), 16, 0, 0); } while (0)
; #define PG8_LDA(dst, b, h) do { if constexpr (FP8) { _Pragma("unroll") for (int m = 0; m < 4; ++m) dst##8[m] = PG8_LD8(lds + PG8_SA(b, h) + aoff + m * 2048); } \
;         else { _Pragma("unroll") for (int m = 0; m < 4; ++m) _Pragma("unroll") for (int k = 0; k < 2; ++k) dst[m][k] = *(const LAS bf16x8*)(lds + PG8_SA(b, h) + aoff + m * 2048 + k * 1024); } } while (0)
; #define PG8_WAIT_V(n) asm volatile("s_waitcnt vmcnt(" #n ")" ::: "memory")
; #define PG8_WAIT_L(n) asm volatile("s_waitcnt lgkmcnt(" #n ")" ::: "memory")
; #define PG8_BAR __builtin_amdgcn_s_barrier()
; #define PG8_SCHED __builtin_amdgcn_sched_barrier(0)
; template <class Epi, class Sched, bool ALIGN_EPI, bool SP2, bool FP8 = false>
; __device__ __forceinline__ void gemm_phase(LAS unsigned char* lds, const int K, const Sched& S, const Epi& E) {
;     ...
;             PG8_LDA(At, 1, 1); PG8_STAGE(PG8_SB(1, 0), b3, voffB); PG8_STAGE(PG8_SB(1, 1), b3 + hstep, voffB); PG8_STAGE(PG8_SA(1, 0), a3, vX0);
;             PG8_WAIT_V(8); PG8_WAIT_L(0); PG8_BAR; PG8_MMA(1, 0, At, B0); PG8_MMA(1, 1, At, B1); PG8_BAR; PG8_SCHED;
;         }
;         if constexpr (ALIGN_EPI) { if (wr == 0) PG8_BAR; }
	s_add_i32 s50, s70, s35
	v_lshl_add_u64 v[230:231], v[230:231], 0, s[40:41]
	s_mov_b32 m0, s50
	ds_read_b128 v[196:199], v155 offset:49152
	ds_read_b128 v[200:203], v155 offset:50176
	ds_read_b128 v[204:207], v155 offset:51200
	ds_read_b128 v[208:211], v155 offset:52224
	ds_read_b128 v[212:215], v155 offset:53248
	ds_read_b128 v[216:219], v155 offset:54272
	ds_read_b128 v[220:223], v155 offset:55296
	ds_read_b128 v[224:227], v155 offset:56320
	global_load_lds_dwordx4 v[230:231], off
	s_add_i32 m0, s50, 0x2000
	s_add_u32 s6, s6, 0x80080
	v_lshl_add_u64 v[230:231], v[232:233], 0, s[40:41]
	s_addc_u32 s7, s7, 0
	s_add_i32 s50, s71, s35
	global_load_lds_dwordx4 v[230:231], off
	v_lshl_add_u64 v[230:231], s[6:7], 0, v[132:133]
	s_mov_b32 m0, s50
	v_lshl_add_u64 v[228:229], v[228:229], 0, s[40:41]
	global_load_lds_dwordx4 v[230:231], off
	v_lshl_add_u64 v[230:231], s[6:7], 0, v[134:135]
	s_add_i32 m0, s50, 0x2000
	s_nop 0
	global_load_lds_dwordx4 v[230:231], off
	v_lshl_add_u64 v[230:231], v[234:235], 0, s[40:41]
	s_mov_b32 m0, s58
	s_nop 0
	global_load_lds_dwordx4 v[230:231], off
	s_mov_b32 m0, s59
	s_nop 0
	global_load_lds_dwordx4 v[228:229], off
	s_waitcnt vmcnt(8)
	s_waitcnt lgkmcnt(0)
	s_setprio 1
	s_barrier
	v_mfma_f32_16x16x32_bf16 v[62:65], v[162:165], v[196:199], v[62:65]
	v_mfma_f32_16x16x32_bf16 v[58:61], v[170:173], v[196:199], v[58:61]
	v_mfma_f32_16x16x32_bf16 v[46:49], v[162:165], v[204:207], v[46:49]
	v_mfma_f32_16x16x32_bf16 v[42:45], v[170:173], v[204:207], v[42:45]
	v_mfma_f32_16x16x32_bf16 v[22:25], v[162:165], v[212:215], v[22:25]
	v_mfma_f32_16x16x32_bf16 v[18:21], v[170:173], v[212:215], v[18:21]
	v_mfma_f32_16x16x32_bf16 v[6:9], v[162:165], v[220:223], v[6:9]
	v_mfma_f32_16x16x32_bf16 v[2:5], v[170:173], v[220:223], v[2:5]
	v_mfma_f32_16x16x32_bf16 v[62:65], v[166:169], v[200:203], v[62:65]
	v_mfma_f32_16x16x32_bf16 v[58:61], v[174:177], v[200:203], v[58:61]
	v_mfma_f32_16x16x32_bf16 v[46:49], v[166:169], v[208:211], v[46:49]
	v_mfma_f32_16x16x32_bf16 v[42:45], v[174:177], v[208:211], v[42:45]
	v_mfma_f32_16x16x32_bf16 v[22:25], v[166:169], v[216:219], v[22:25]
	v_mfma_f32_16x16x32_bf16 v[18:21], v[174:177], v[216:219], v[18:21]
	v_mfma_f32_16x16x32_bf16 v[6:9], v[166:169], v[224:227], v[6:9]
	v_mfma_f32_16x16x32_bf16 v[2:5], v[174:177], v[224:227], v[2:5]
	v_mfma_f32_16x16x32_bf16 v[54:57], v[178:181], v[196:199], v[54:57]
	v_mfma_f32_16x16x32_bf16 v[50:53], v[186:189], v[196:199], v[50:53]
	v_mfma_f32_16x16x32_bf16 v[30:33], v[178:181], v[204:207], v[30:33]
	v_mfma_f32_16x16x32_bf16 v[26:29], v[186:189], v[204:207], v[26:29]
	v_mfma_f32_16x16x32_bf16 v[34:37], v[178:181], v[212:215], v[34:37]
	v_mfma_f32_16x16x32_bf16 v[38:41], v[186:189], v[212:215], v[38:41]
	v_mfma_f32_16x16x32_bf16 v[10:13], v[178:181], v[220:223], v[10:13]
	v_mfma_f32_16x16x32_bf16 v[14:17], v[186:189], v[220:223], v[14:17]
	v_mfma_f32_16x16x32_bf16 v[54:57], v[182:185], v[200:203], v[54:57]
	v_mfma_f32_16x16x32_bf16 v[50:53], v[192:195], v[200:203], v[50:53]
	v_mfma_f32_16x16x32_bf16 v[30:33], v[182:185], v[208:211], v[30:33]
	v_mfma_f32_16x16x32_bf16 v[26:29], v[192:195], v[208:211], v[26:29]
	v_mfma_f32_16x16x32_bf16 v[34:37], v[182:185], v[216:219], v[34:37]
	v_mfma_f32_16x16x32_bf16 v[38:41], v[192:195], v[216:219], v[38:41]
	v_mfma_f32_16x16x32_bf16 v[10:13], v[182:185], v[224:227], v[10:13]
	v_mfma_f32_16x16x32_bf16 v[14:17], v[192:195], v[224:227], v[14:17]
	s_setprio 0
	s_barrier
	s_add_i32 s69, s69, 2
	s_add_u32 s4, s4, 0x100
	s_addc_u32 s5, s5, 0
	s_cmp_gt_u32 s69, 29
	s_cbranch_scc0 .LBB0_883
	s_and_b64 vcc, exec, s[44:45]
	s_cbranch_vccz .LBB0_886
	s_barrier

; #define LAS __attribute__((address_space(3)))
; __device__ __forceinline__ void cvt_fill_g(const Frame& F) { LAS float* gl = (LAS float*)(F.lds + BG_G_OFF); for (int i = F.tid; i < DM; i += NTHREADS) gl[i] = F.g_moe[i] * WSCALE; __syncthreads(); }
;     __device__ __forceinline__ void init(const Frame& F_, int first_item, int n_items) { init(F_, first_item, n_items, F_.vcu, F_.G); }
; __global__ void __launch_bounds__(NTHREADS, 2) mk_fwd(Args args) {
;     ...
;         if (F.G == 256 && blockIdx.x >= 128) {
;             cvt_fill_g(F);
;             Bg bg; bg.init(F, CVT_ITEMS - CVT_P9_ITEMS - CVT_P4_ITEMS, CVT_P4_ITEMS, (int)blockIdx.x - 128, 128); bg.drain();
.LBB0_892:
	global_load_dword v6, v[2:3], off
	v_add_u32_e32 v5, 0x200, v5
	v_cmp_lt_u32_e32 vcc, s3, v5
	v_lshl_add_u64 v[2:3], v[2:3], 0, s[4:5]
	s_or_b64 s[0:1], vcc, s[0:1]
	s_waitcnt vmcnt(0)
	v_mul_f32_e32 v6, 0x42800000, v6
	ds_write_b32 v4, v6
	v_add_u32_e32 v4, 0x800, v4
	s_andn2_b64 exec, exec, s[0:1]
	s_cbranch_execnz .LBB0_892
	s_or_b64 exec, exec, s[0:1]
	v_readlane_b32 s1, v254, 8
	s_lshl_b32 s0, s2, 2
	s_lshr_b32 s1, s1, 7
	s_add_i32 s3, s0, s1
	s_addk_i32 s3, 0x4600
	s_cmpk_gt_i32 s3, 0x57ff
	s_mov_b32 s34, 0
	s_waitcnt lgkmcnt(0)
	s_barrier
	s_cbranch_scc1 .LBB0_895
	s_sub_i32 s0, 0x59ff, s3
	s_ashr_i32 s1, s0, 31
	s_lshr_b32 s1, s1, 23
	s_add_i32 s0, s0, s1
	s_ashr_i32 s0, s0, 9
	s_lshl_b32 s34, s0, 1

; #define LAS __attribute__((address_space(3)))
; __device__ __forceinline__ unsigned cvtpk(float lo, float hi) { typedef __bf16 bf16x2_t __attribute__((ext_vector_type(2))); f32x2 v = {lo, hi}; bf16x2_t b = __builtin_convertvector(v, bf16x2_t); return __builtin_bit_cast(unsigned, b); }
; __device__ __forceinline__ s16x4 vtr(const LAS unsigned char* p) { return __builtin_bit_cast(s16x4, __builtin_amdgcn_ds_read_tr16_b64_v4i16((LAS v4i16_t*)p)); }
; template <int D, bool MASK, bool BIAS, bool SINK, bool REV, bool O8, class BG>
; __device__ __forceinline__ void attn_unit(const Prm& P, LAS unsigned char* lds, BG& bg) {
;     ...
;             float sacc = 0.f;
; #pragma unroll
;             for (int r = 0; r < 16; ++r) { p0[r] = __builtin_amdgcn_exp2f(p0[r]); p1[r] = __builtin_amdgcn_exp2f(p1[r]); sacc += p0[r] + p1[r]; }
;             l_reg += sacc;
;             u32x4 pw[4];
; #pragma unroll
;             for (int q = 0; q < 4; ++q) { pw[0][q] = cvtpk(p0[2 * q], p0[2 * q + 1]); pw[1][q] = cvtpk(p0[8 + 2 * q], p0[9 + 2 * q]); pw[2][q] = cvtpk(p1[2 * q], p1[2 * q + 1]); pw[3][q] = cvtpk(p1[8 + 2 * q], p1[9 + 2 * q]); }
;             const LAS unsigned char* vs = lds + VOFF + s * KSLOT + ((lane >> 4) & 1) * 32 + (lane & 3) * 8 + (4 * hi + ((lane & 15) >> 2)) * 64;
; #pragma unroll
;             for (int d = 0; d < NDB; ++d)
; #pragma unroll
;                 for (int k4 = 0; k4 < 4; ++k4) {
;                     const s16x4 vlo = vtr(vs + d * 4096 + k4 * 1024), vhi = vtr(vs + d * 4096 + k4 * 1024 + 512);
;                     const bf16x8 vf = (bf16x8){vlo[0], vlo[1], vlo[2], vlo[3], vhi[0], vhi[1], vhi[2], vhi[3]};
;                     o[d] = __builtin_amdgcn_mfma_f32_32x32x16_bf16(__builtin_bit_cast(bf16x8, pw[k4]), vf, o[d], 0, 0, 0);
;                 }
.LBB0_940:
	v_exp_f32_e32 v2, v84
	v_exp_f32_e32 v135, v68
	v_exp_f32_e32 v151, v85
	v_exp_f32_e32 v156, v69
	v_exp_f32_e32 v86, v86
	v_exp_f32_e32 v157, v70
	v_exp_f32_e32 v87, v87
	v_exp_f32_e32 v158, v71
	v_add_f32_e32 v68, v135, v2
	v_exp_f32_e32 v159, v88
	v_exp_f32_e32 v160, v72
	v_add_f32_e32 v68, 0, v68
	v_add_f32_e32 v69, v156, v151
	v_exp_f32_e32 v70, v89
	v_exp_f32_e32 v88, v73
	v_add_f32_e32 v68, v69, v68
	v_add_f32_e32 v69, v157, v86
	v_add_f32_e32 v68, v69, v68
	v_add_f32_e32 v69, v158, v87
	v_add_f32_e32 v71, v69, v68
	v_add_f32_e32 v89, v160, v159
	v_pk_add_f32 v[68:69], v[88:89], v[70:71]
	v_exp_f32_e32 v71, v90
	v_pk_add_f32 v[72:73], v[68:69], v[68:69] op_sel_hi:[0,1]
	v_exp_f32_e32 v89, v74
	v_exp_f32_e32 v72, v91
	v_exp_f32_e32 v90, v75
	v_exp_f32_e32 v161, v76
	v_add_f32_e32 v91, v89, v71
	v_cvt_pk_bf16_f32 v70, v159, v70
	v_pk_add_f32 v[68:69], v[90:91], v[72:73]
	v_exp_f32_e32 v91, v92
	v_pk_add_f32 v[84:85], v[68:69], v[68:69] op_sel_hi:[0,1]
	v_exp_f32_e32 v84, v93
	v_exp_f32_e32 v92, v77
	v_add_f32_e32 v93, v161, v91
	v_exp_f32_e32 v77, v94
	v_exp_f32_e32 v94, v79
	v_pk_add_f32 v[68:69], v[92:93], v[84:85]
	v_exp_f32_e32 v93, v78
	v_pk_add_f32 v[152:153], v[68:69], v[68:69] op_sel_hi:[0,1]
	v_exp_f32_e32 v152, v95
	v_cvt_pk_bf16_f32 v71, v71, v72
	v_add_f32_e32 v95, v93, v77
	v_cvt_pk_bf16_f32 v76, v91, v84
	v_pk_add_f32 v[68:69], v[94:95], v[152:153]
	v_exp_f32_e32 v95, v96
	v_pk_add_f32 v[78:79], v[68:69], v[68:69] op_sel_hi:[0,1]
	v_exp_f32_e32 v153, v80
	v_exp_f32_e32 v78, v97
	v_exp_f32_e32 v96, v81
	v_cvt_pk_bf16_f32 v77, v77, v152
	v_add_f32_e32 v97, v153, v95
	v_cvt_pk_bf16_f32 v80, v161, v92
	v_pk_add_f32 v[68:69], v[96:97], v[78:79]
	v_exp_f32_e32 v97, v98
	v_pk_add_f32 v[154:155], v[68:69], v[68:69] op_sel_hi:[0,1]
	v_cvt_pk_bf16_f32 v68, v2, v151
	v_add_u32_e32 v2, s74, v1
	v_cvt_pk_bf16_f32 v69, v86, v87
	s_nop 0
	ds_read_b64_tr_b16 v[72:73], v2 offset:32768
	ds_read_b64_tr_b16 v[74:75], v2 offset:33280
	v_exp_f32_e32 v154, v99
	s_waitcnt lgkmcnt(0)
	v_mfma_f32_32x32x16_bf16 v[52:67], v[68:71], v[72:75], v[52:67]
	ds_read_b64_tr_b16 v[84:85], v2 offset:33792
	ds_read_b64_tr_b16 v[86:87], v2 offset:34304
	v_cvt_pk_bf16_f32 v78, v95, v78
	v_cvt_pk_bf16_f32 v79, v97, v154
	v_cvt_pk_bf16_f32 v72, v135, v156
	v_cvt_pk_bf16_f32 v73, v157, v158
	v_cvt_pk_bf16_f32 v74, v160, v88
	v_cvt_pk_bf16_f32 v75, v89, v90
	s_waitcnt lgkmcnt(0)
	v_mfma_f32_32x32x16_bf16 v[52:67], v[76:79], v[84:87], v[52:67]
	ds_read_b64_tr_b16 v[84:85], v2 offset:34816
	ds_read_b64_tr_b16 v[86:87], v2 offset:35328
	v_exp_f32_e32 v95, v82
	v_exp_f32_e32 v98, v83
	ds_read_b64_tr_b16 v[88:89], v2 offset:35840
	ds_read_b64_tr_b16 v[90:91], v2 offset:36352
	v_cvt_pk_bf16_f32 v81, v93, v94
	v_cvt_pk_bf16_f32 v82, v153, v96
	v_cvt_pk_bf16_f32 v83, v95, v98
	s_waitcnt lgkmcnt(2)
	v_mfma_f32_32x32x16_bf16 v[52:67], v[72:75], v[84:87], v[52:67]
	v_add_f32_e32 v99, v95, v97
	s_add_i32 s73, s73, 1
	v_add_u32_e32 v147, 64, v147
	v_add_u32_e32 v150, 64, v150
	s_cmp_eq_u32 s73, 4
	s_mov_b64 s[44:45], 0
	s_waitcnt lgkmcnt(0)
	v_mfma_f32_32x32x16_bf16 v[52:67], v[80:83], v[88:91], v[52:67]
	ds_read_b64_tr_b16 v[84:85], v2 offset:36864
	ds_read_b64_tr_b16 v[86:87], v2 offset:37376
	ds_read_b64_tr_b16 v[88:89], v2 offset:37888
	ds_read_b64_tr_b16 v[90:91], v2 offset:38400
	s_waitcnt lgkmcnt(2)
	v_mfma_f32_32x32x16_bf16 v[36:51], v[68:71], v[84:87], v[36:51]
	s_waitcnt lgkmcnt(0)
	v_mfma_f32_32x32x16_bf16 v[36:51], v[76:79], v[88:91], v[36:51]
	ds_read_b64_tr_b16 v[84:85], v2 offset:38912
	ds_read_b64_tr_b16 v[86:87], v2 offset:39424
	ds_read_b64_tr_b16 v[88:89], v2 offset:39936
	ds_read_b64_tr_b16 v[90:91], v2 offset:40448
	s_waitcnt lgkmcnt(2)
	v_mfma_f32_32x32x16_bf16 v[36:51], v[72:75], v[84:87], v[36:51]
	s_waitcnt lgkmcnt(0)
	v_mfma_f32_32x32x16_bf16 v[36:51], v[80:83], v[88:91], v[36:51]
	ds_read_b64_tr_b16 v[84:85], v2 offset:40960
	ds_read_b64_tr_b16 v[86:87], v2 offset:41472
	ds_read_b64_tr_b16 v[88:89], v2 offset:41984
	ds_read_b64_tr_b16 v[90:91], v2 offset:42496
	s_waitcnt lgkmcnt(2)
	v_mfma_f32_32x32x16_bf16 v[20:35], v[68:71], v[84:87], v[20:35]
	s_waitcnt lgkmcnt(0)
	v_mfma_f32_32x32x16_bf16 v[20:35], v[76:79], v[88:91], v[20:35]
	ds_read_b64_tr_b16 v[84:85], v2 offset:43008
	ds_read_b64_tr_b16 v[86:87], v2 offset:43520
	ds_read_b64_tr_b16 v[88:89], v2 offset:44032
	ds_read_b64_tr_b16 v[90:91], v2 offset:44544
	s_waitcnt lgkmcnt(2)
	v_mfma_f32_32x32x16_bf16 v[20:35], v[72:75], v[84:87], v[20:35]
	s_waitcnt lgkmcnt(0)
	v_mfma_f32_32x32x16_bf16 v[20:35], v[80:83], v[88:91], v[20:35]
	ds_read_b64_tr_b16 v[84:85], v2 offset:45056
	ds_read_b64_tr_b16 v[86:87], v2 offset:45568
	ds_read_b64_tr_b16 v[88:89], v2 offset:46080
	ds_read_b64_tr_b16 v[90:91], v2 offset:46592
	s_waitcnt lgkmcnt(2)
	v_mfma_f32_32x32x16_bf16 v[4:19], v[68:71], v[84:87], v[4:19]
	s_waitcnt lgkmcnt(0)
	v_mfma_f32_32x32x16_bf16 v[4:19], v[76:79], v[88:91], v[4:19]
	ds_read_b64_tr_b16 v[68:69], v2 offset:47104
	ds_read_b64_tr_b16 v[70:71], v2 offset:47616
	ds_read_b64_tr_b16 v[76:77], v2 offset:48128
	ds_read_b64_tr_b16 v[78:79], v2 offset:48640
	s_waitcnt lgkmcnt(2)
	v_mfma_f32_32x32x16_bf16 v[4:19], v[72:75], v[68:71], v[4:19]
	v_add_f32_e64 v68, v98, v154
	v_add_f32_e64 v69, v99, v155
	v_add_f32_e32 v2, v68, v69
	v_add_f32_e32 v149, v149, v2
	s_waitcnt lgkmcnt(0)
	v_mfma_f32_32x32x16_bf16 v[4:19], v[80:83], v[76:79], v[4:19]
	s_cbranch_scc1 .LBB0_951

; #define PG8_STAGE(bufoff, gbase, voff) do { _Pragma("unroll") for (int _i = 0; _i < 2; ++_i) \
;         __builtin_amdgcn_global_load_lds((const unsigned*)((const char*)(gbase) + (voff)[_i]), (LAS unsigned*)(lds + (bufoff) + ldsw + _i * 8192), 16, 0, 0); } while (0)
; #define PG8_LDA(dst, b, h) do { if constexpr (FP8) { _Pragma("unroll") for (int m = 0; m < 4; ++m) dst##8[m] = PG8_LD8(lds + PG8_SA(b, h) + aoff + m * 2048); } \
;         else { _Pragma("unroll") for (int m = 0; m < 4; ++m) _Pragma("unroll") for (int k = 0; k < 2; ++k) dst[m][k] = *(const LAS bf16x8*)(lds + PG8_SA(b, h) + aoff + m * 2048 + k * 1024); } } while (0)
; #define PG8_LDB(dst, b, h) do { if constexpr (FP8) { _Pragma("unroll") for (int n = 0; n < 2; ++n) dst##8[n] = PG8_LD8(lds + PG8_SB(b, h) + boff + n * 2048); } \
;         else { _Pragma("unroll") for (int n = 0; n < 2; ++n) _Pragma("unroll") for (int k = 0; k < 2; ++k) dst[n][k] = *(const LAS bf16x8*)(lds + PG8_SB(b, h) + boff + n * 2048 + k * 1024); } } while (0)
; #define PG8_WAIT_V(n) asm volatile("s_waitcnt vmcnt(" #n ")" ::: "memory")
; #define PG8_WAIT_L(n) asm volatile("s_waitcnt lgkmcnt(" #n ")" ::: "memory")
; template <class Epi, class Sched, bool ALIGN_EPI, bool SP2, bool FP8 = false>
; __device__ __forceinline__ void gemm_phase(LAS unsigned char* lds, const int K, const Sched& S, const Epi& E) {
;     ...
;         for (int t = 0; t < nt; t += 2) {
;             const bool last = (t == nt - 2);
;             const char* a1 = cA + (size_t)(t + 1) * kstep;
;             const char* a2 = last ? nA : cA + (size_t)(t + 2) * kstep; const char* b2 = last ? nB : cB + (size_t)(t + 2) * kstep;
;             const char* a3 = a2 + kstep; const char* b3 = b2 + kstep;
;             unsigned vX0[2], vX1[2];
; #pragma unroll
;             for (int i = 0; i < 2; ++i) { vX0[i] = last ? vAn[0][i] : vAc[0][i]; vX1[i] = last ? vAn[1][i] : vAc[1][i]; }
;             PG8_LDB(B0, 0, 0); PG8_LDB(B1, 0, 1); PG8_SCHED; PG8_LDA(At, 0, 0); PG8_STAGE(PG8_SA(1, 1), a1, vAc[1]);
;             PG8_WAIT_V(8); PG8_WAIT_L(0); PG8_BAR; PG8_MMA(0, 0, At, B0); PG8_MMA(0, 1, At, B1); PG8_BAR; PG8_SCHED;
;             PG8_LDA(At, 0, 1); PG8_STAGE(PG8_SB(0, 0), b2, voffB); PG8_STAGE(PG8_SB(0, 1), b2 + hstep, voffB); PG8_STAGE(PG8_SA(0, 0), a2, vX0);
;             PG8_WAIT_V(8); PG8_WAIT_L(0); PG8_BAR; PG8_MMA(1, 0, At, B0); PG8_MMA(1, 1, At, B1); PG8_BAR; PG8_SCHED;
.LBB0_1025:
	ds_read_b128 v[140:143], v182
	ds_read_b128 v[144:147], v182 offset:1024
	ds_read_b128 v[148:151], v182 offset:2048
	ds_read_b128 v[160:163], v182 offset:3072
	ds_read_b128 v[164:167], v183
	ds_read_b128 v[168:171], v183 offset:1024
	ds_read_b128 v[172:175], v183 offset:2048
	ds_read_b128 v[192:195], v183 offset:3072
	s_add_u32 s56, s30, s50
	s_addc_u32 s57, s31, s51
	s_add_u32 s58, s56, 0x23000100
	s_addc_u32 s59, s57, 0
	s_add_u32 s69, s45, s50
	s_addc_u32 s70, s49, s51
	s_cmpk_eq_i32 s50, 0x300
	s_cselect_b64 vcc, -1, 0
	s_and_b64 s[56:57], vcc, exec
	v_cndmask_b32_e32 v158, v135, v186, vcc
	s_cselect_b32 s59, s9, s59
	s_cselect_b32 s58, s8, s58
	v_cndmask_b32_e32 v131, v130, v187, vcc
	v_cndmask_b32_e32 v152, v134, v188, vcc
	v_cndmask_b32_e32 v133, v132, v189, vcc
	s_cselect_b32 s57, s47, s70
	s_cselect_b32 s56, s46, s69
	v_lshl_add_u64 v[176:177], v[138:139], 0, s[50:51]
	s_add_i32 m0, s53, 0xc000
	ds_read_b128 v[196:199], v184
	ds_read_b128 v[200:203], v184 offset:1024
	ds_read_b128 v[204:207], v184 offset:2048
	ds_read_b128 v[208:211], v184 offset:3072
	ds_read_b128 v[212:215], v184 offset:4096
	ds_read_b128 v[216:219], v184 offset:5120
	ds_read_b128 v[220:223], v184 offset:6144
	ds_read_b128 v[224:227], v184 offset:7168
	global_load_lds_dwordx4 v[176:177], off
	v_lshl_add_u64 v[176:177], v[136:137], 0, s[50:51]
	s_add_i32 m0, s53, 0xe000
	s_nop 0
	global_load_lds_dwordx4 v[176:177], off
	s_waitcnt vmcnt(8)
	s_waitcnt lgkmcnt(0)
	s_setprio 1
	s_barrier
	v_mfma_f32_16x16x32_bf16 v[126:129], v[140:143], v[196:199], v[126:129]
	v_mfma_f32_16x16x32_bf16 v[122:125], v[148:151], v[196:199], v[122:125]
	v_mfma_f32_16x16x32_bf16 v[110:113], v[140:143], v[204:207], v[110:113]
	v_mfma_f32_16x16x32_bf16 v[106:109], v[148:151], v[204:207], v[106:109]
	v_mfma_f32_16x16x32_bf16 v[94:97], v[140:143], v[212:215], v[94:97]
	v_mfma_f32_16x16x32_bf16 v[90:93], v[148:151], v[212:215], v[90:93]
	v_mfma_f32_16x16x32_bf16 v[78:81], v[140:143], v[220:223], v[78:81]
	v_mfma_f32_16x16x32_bf16 v[74:77], v[148:151], v[220:223], v[74:77]
	v_mfma_f32_16x16x32_bf16 v[126:129], v[144:147], v[200:203], v[126:129]
	v_mfma_f32_16x16x32_bf16 v[122:125], v[160:163], v[200:203], v[122:125]
	v_mfma_f32_16x16x32_bf16 v[110:113], v[144:147], v[208:211], v[110:113]
	v_mfma_f32_16x16x32_bf16 v[106:109], v[160:163], v[208:211], v[106:109]
	v_mfma_f32_16x16x32_bf16 v[94:97], v[144:147], v[216:219], v[94:97]
	v_mfma_f32_16x16x32_bf16 v[90:93], v[160:163], v[216:219], v[90:93]
	v_mfma_f32_16x16x32_bf16 v[78:81], v[144:147], v[224:227], v[78:81]
	v_mfma_f32_16x16x32_bf16 v[74:77], v[160:163], v[224:227], v[74:77]
	v_mfma_f32_16x16x32_bf16 v[118:121], v[164:167], v[196:199], v[118:121]
	v_mfma_f32_16x16x32_bf16 v[114:117], v[172:175], v[196:199], v[114:117]
	v_mfma_f32_16x16x32_bf16 v[102:105], v[164:167], v[204:207], v[102:105]
	v_mfma_f32_16x16x32_bf16 v[98:101], v[172:175], v[204:207], v[98:101]
	v_mfma_f32_16x16x32_bf16 v[86:89], v[164:167], v[212:215], v[86:89]
	v_mfma_f32_16x16x32_bf16 v[82:85], v[172:175], v[212:215], v[82:85]
	v_mfma_f32_16x16x32_bf16 v[70:73], v[164:167], v[220:223], v[70:73]
	v_mfma_f32_16x16x32_bf16 v[66:69], v[172:175], v[220:223], v[66:69]
	v_mfma_f32_16x16x32_bf16 v[118:121], v[168:171], v[200:203], v[118:121]
	v_mfma_f32_16x16x32_bf16 v[114:117], v[192:195], v[200:203], v[114:117]
	v_mfma_f32_16x16x32_bf16 v[102:105], v[168:171], v[208:211], v[102:105]
	v_mfma_f32_16x16x32_bf16 v[98:101], v[192:195], v[208:211], v[98:101]
	v_mfma_f32_16x16x32_bf16 v[86:89], v[168:171], v[216:219], v[86:89]
	v_mfma_f32_16x16x32_bf16 v[82:85], v[192:195], v[216:219], v[82:85]
	v_mfma_f32_16x16x32_bf16 v[70:73], v[168:171], v[224:227], v[70:73]
	v_mfma_f32_16x16x32_bf16 v[66:69], v[192:195], v[224:227], v[66:69]
	s_setprio 0
	s_barrier
	s_add_i32 s69, s64, s35
	v_lshl_add_u64 v[176:177], s[56:57], 0, v[154:155]
	s_mov_b32 m0, s69
	ds_read_b128 v[196:199], v184 offset:16384
	ds_read_b128 v[200:203], v184 offset:17408
	ds_read_b128 v[204:207], v184 offset:18432
	ds_read_b128 v[208:211], v184 offset:19456
	ds_read_b128 v[212:215], v184 offset:20480
	ds_read_b128 v[216:219], v184 offset:21504
	ds_read_b128 v[220:223], v184 offset:22528
	ds_read_b128 v[224:227], v184 offset:23552
	global_load_lds_dwordx4 v[176:177], off
	s_add_i32 m0, s69, 0x2000
	s_add_u32 s70, s56, 0x20000
	v_lshl_add_u64 v[228:229], s[56:57], 0, v[156:157]
	s_addc_u32 s71, s57, 0
	s_add_i32 s69, s65, s35
	global_load_lds_dwordx4 v[228:229], off
	v_lshl_add_u64 v[230:231], s[70:71], 0, v[154:155]
	s_mov_b32 m0, s69
	v_mov_b32_e32 v153, v159
	global_load_lds_dwordx4 v[230:231], off
	v_lshl_add_u64 v[230:231], s[70:71], 0, v[156:157]
	s_add_i32 m0, s69, 0x2000
	s_nop 0
	global_load_lds_dwordx4 v[230:231], off
	s_mov_b32 m0, s53
	v_lshl_add_u64 v[230:231], s[58:59], 0, v[158:159]
	global_load_lds_dwordx4 v158, s[58:59]
	s_mov_b32 m0, s54
	s_nop 0
	global_load_lds_dwordx4 v152, s[58:59]
	s_waitcnt vmcnt(8)
	s_waitcnt lgkmcnt(0)
	v_lshl_add_u64 v[152:153], s[58:59], 0, v[152:153]
	s_setprio 1
	s_barrier
; #define PG8_STAGE(bufoff, gbase, voff) do { _Pragma("unroll") for (int _i = 0; _i < 2; ++_i) \
;         __builtin_amdgcn_global_load_lds((const unsigned*)((const char*)(gbase) + (voff)[_i]), (LAS unsigned*)(lds + (bufoff) + ldsw + _i * 8192), 16, 0, 0); } while (0)
; #define PG8_LDA(dst, b, h) do { if constexpr (FP8) { _Pragma("unroll") for (int m = 0; m < 4; ++m) dst##8[m] = PG8_LD8(lds + PG8_SA(b, h) + aoff + m * 2048); } \
;         else { _Pragma("unroll") for (int m = 0; m < 4; ++m) _Pragma("unroll") for (int k = 0; k < 2; ++k) dst[m][k] = *(const LAS bf16x8*)(lds + PG8_SA(b, h) + aoff + m * 2048 + k * 1024); } } while (0)
; #define PG8_LDB(dst, b, h) do { if constexpr (FP8) { _Pragma("unroll") for (int n = 0; n < 2; ++n) dst##8[n] = PG8_LD8(lds + PG8_SB(b, h) + boff + n * 2048); } \
;         else { _Pragma("unroll") for (int n = 0; n < 2; ++n) _Pragma("unroll") for (int k = 0; k < 2; ++k) dst[n][k] = *(const LAS bf16x8*)(lds + PG8_SB(b, h) + boff + n * 2048 + k * 1024); } } while (0)
; #define PG8_WAIT_V(n) asm volatile("s_waitcnt vmcnt(" #n ")" ::: "memory")
; #define PG8_WAIT_L(n) asm volatile("s_waitcnt lgkmcnt(" #n ")" ::: "memory")
; #define PG8_BAR __builtin_amdgcn_s_barrier()
; #define PG8_SCHED __builtin_amdgcn_sched_barrier(0)
; template <class Epi, class Sched, bool ALIGN_EPI, bool SP2, bool FP8 = false>
; __device__ __forceinline__ void gemm_phase(LAS unsigned char* lds, const int K, const Sched& S, const Epi& E) {
;     ...
;             PG8_WAIT_V(8); PG8_WAIT_L(0); PG8_BAR; PG8_MMA(1, 0, At, B0); PG8_MMA(1, 1, At, B1); PG8_BAR; PG8_SCHED;
;             PG8_LDB(B0, 1, 0); PG8_LDB(B1, 1, 1); PG8_SCHED; PG8_LDA(At, 1, 0); PG8_STAGE(PG8_SA(0, 1), a2, vX1);
;             PG8_WAIT_V(8); PG8_WAIT_L(0); PG8_BAR; PG8_MMA(0, 0, At, B0); PG8_MMA(0, 1, At, B1); PG8_BAR; PG8_SCHED;
	v_mfma_f32_16x16x32_bf16 v[62:65], v[140:143], v[196:199], v[62:65]
	v_mfma_f32_16x16x32_bf16 v[58:61], v[148:151], v[196:199], v[58:61]
	v_mfma_f32_16x16x32_bf16 v[46:49], v[140:143], v[204:207], v[46:49]
	v_mfma_f32_16x16x32_bf16 v[42:45], v[148:151], v[204:207], v[42:45]
	v_mfma_f32_16x16x32_bf16 v[22:25], v[140:143], v[212:215], v[22:25]
	v_mfma_f32_16x16x32_bf16 v[18:21], v[148:151], v[212:215], v[18:21]
	v_mfma_f32_16x16x32_bf16 v[6:9], v[140:143], v[220:223], v[6:9]
	v_mfma_f32_16x16x32_bf16 v[2:5], v[148:151], v[220:223], v[2:5]
	v_mfma_f32_16x16x32_bf16 v[62:65], v[144:147], v[200:203], v[62:65]
	v_mfma_f32_16x16x32_bf16 v[58:61], v[160:163], v[200:203], v[58:61]
	v_mfma_f32_16x16x32_bf16 v[46:49], v[144:147], v[208:211], v[46:49]
	v_mfma_f32_16x16x32_bf16 v[42:45], v[160:163], v[208:211], v[42:45]
	v_mfma_f32_16x16x32_bf16 v[22:25], v[144:147], v[216:219], v[22:25]
	v_mfma_f32_16x16x32_bf16 v[18:21], v[160:163], v[216:219], v[18:21]
	v_mfma_f32_16x16x32_bf16 v[6:9], v[144:147], v[224:227], v[6:9]
	v_mfma_f32_16x16x32_bf16 v[2:5], v[160:163], v[224:227], v[2:5]
	v_mfma_f32_16x16x32_bf16 v[54:57], v[164:167], v[196:199], v[54:57]
	v_mfma_f32_16x16x32_bf16 v[50:53], v[172:175], v[196:199], v[50:53]
	v_mfma_f32_16x16x32_bf16 v[38:41], v[164:167], v[204:207], v[38:41]
	v_mfma_f32_16x16x32_bf16 v[34:37], v[172:175], v[204:207], v[34:37]
	v_mfma_f32_16x16x32_bf16 v[30:33], v[164:167], v[212:215], v[30:33]
	v_mfma_f32_16x16x32_bf16 v[26:29], v[172:175], v[212:215], v[26:29]
	v_mfma_f32_16x16x32_bf16 v[14:17], v[164:167], v[220:223], v[14:17]
	v_mfma_f32_16x16x32_bf16 v[10:13], v[172:175], v[220:223], v[10:13]
	v_mfma_f32_16x16x32_bf16 v[54:57], v[168:171], v[200:203], v[54:57]
	v_mfma_f32_16x16x32_bf16 v[50:53], v[192:195], v[200:203], v[50:53]
	v_mfma_f32_16x16x32_bf16 v[38:41], v[168:171], v[208:211], v[38:41]
	v_mfma_f32_16x16x32_bf16 v[34:37], v[192:195], v[208:211], v[34:37]
	v_mfma_f32_16x16x32_bf16 v[30:33], v[168:171], v[216:219], v[30:33]
	v_mfma_f32_16x16x32_bf16 v[26:29], v[192:195], v[216:219], v[26:29]
	v_mfma_f32_16x16x32_bf16 v[14:17], v[168:171], v[224:227], v[14:17]
	v_mfma_f32_16x16x32_bf16 v[10:13], v[192:195], v[224:227], v[10:13]
	s_setprio 0
	s_barrier
	s_add_i32 s69, 0, 0x18000
	v_add_u32_e32 v158, s69, v180
	s_add_i32 s70, 0, 0x1c000
	ds_read_b128 v[140:143], v158
	ds_read_b128 v[144:147], v158 offset:1024
	ds_read_b128 v[148:151], v158 offset:2048
	ds_read_b128 v[160:163], v158 offset:3072
	v_add_u32_e32 v158, s70, v180
	ds_read_b128 v[164:167], v158
	ds_read_b128 v[168:171], v158 offset:1024
	ds_read_b128 v[172:175], v158 offset:2048
	ds_read_b128 v[192:195], v158 offset:3072
	s_mov_b32 m0, s55
	ds_read_b128 v[196:199], v184 offset:32768
	ds_read_b128 v[200:203], v184 offset:33792
	ds_read_b128 v[204:207], v184 offset:34816
	ds_read_b128 v[208:211], v184 offset:35840
	ds_read_b128 v[212:215], v184 offset:36864
	ds_read_b128 v[216:219], v184 offset:37888
	ds_read_b128 v[220:223], v184 offset:38912
	ds_read_b128 v[224:227], v184 offset:39936
	global_load_lds_dwordx4 v131, s[58:59]
	s_mov_b32 m0, s60
	s_nop 0
	global_load_lds_dwordx4 v133, s[58:59]
	s_waitcnt vmcnt(8)
	s_waitcnt lgkmcnt(0)
	s_setprio 1
	s_barrier
	v_mfma_f32_16x16x32_bf16 v[126:129], v[140:143], v[196:199], v[126:129]
	v_mfma_f32_16x16x32_bf16 v[122:125], v[148:151], v[196:199], v[122:125]
	v_mfma_f32_16x16x32_bf16 v[110:113], v[140:143], v[204:207], v[110:113]
	v_mfma_f32_16x16x32_bf16 v[106:109], v[148:151], v[204:207], v[106:109]
	v_mfma_f32_16x16x32_bf16 v[94:97], v[140:143], v[212:215], v[94:97]
	v_mfma_f32_16x16x32_bf16 v[90:93], v[148:151], v[212:215], v[90:93]
	v_mfma_f32_16x16x32_bf16 v[78:81], v[140:143], v[220:223], v[78:81]
	v_mfma_f32_16x16x32_bf16 v[74:77], v[148:151], v[220:223], v[74:77]
	v_mfma_f32_16x16x32_bf16 v[126:129], v[144:147], v[200:203], v[126:129]
	v_mfma_f32_16x16x32_bf16 v[122:125], v[160:163], v[200:203], v[122:125]
	v_mfma_f32_16x16x32_bf16 v[110:113], v[144:147], v[208:211], v[110:113]
	v_mfma_f32_16x16x32_bf16 v[106:109], v[160:163], v[208:211], v[106:109]
	v_mfma_f32_16x16x32_bf16 v[94:97], v[144:147], v[216:219], v[94:97]
	v_mfma_f32_16x16x32_bf16 v[90:93], v[160:163], v[216:219], v[90:93]
	v_mfma_f32_16x16x32_bf16 v[78:81], v[144:147], v[224:227], v[78:81]
	v_mfma_f32_16x16x32_bf16 v[74:77], v[160:163], v[224:227], v[74:77]
	v_mfma_f32_16x16x32_bf16 v[118:121], v[164:167], v[196:199], v[118:121]
	v_mfma_f32_16x16x32_bf16 v[114:117], v[172:175], v[196:199], v[114:117]
	v_mfma_f32_16x16x32_bf16 v[102:105], v[164:167], v[204:207], v[102:105]
	v_mfma_f32_16x16x32_bf16 v[98:101], v[172:175], v[204:207], v[98:101]
	v_mfma_f32_16x16x32_bf16 v[86:89], v[164:167], v[212:215], v[86:89]
	v_mfma_f32_16x16x32_bf16 v[82:85], v[172:175], v[212:215], v[82:85]
	v_mfma_f32_16x16x32_bf16 v[70:73], v[164:167], v[220:223], v[70:73]
	v_mfma_f32_16x16x32_bf16 v[66:69], v[172:175], v[220:223], v[66:69]
	v_mfma_f32_16x16x32_bf16 v[118:121], v[168:171], v[200:203], v[118:121]
	v_mfma_f32_16x16x32_bf16 v[114:117], v[192:195], v[200:203], v[114:117]
	v_mfma_f32_16x16x32_bf16 v[102:105], v[168:171], v[208:211], v[102:105]
	v_mfma_f32_16x16x32_bf16 v[98:101], v[192:195], v[208:211], v[98:101]
	v_mfma_f32_16x16x32_bf16 v[86:89], v[168:171], v[216:219], v[86:89]
	v_mfma_f32_16x16x32_bf16 v[82:85], v[192:195], v[216:219], v[82:85]
	v_mfma_f32_16x16x32_bf16 v[70:73], v[168:171], v[224:227], v[70:73]
	v_mfma_f32_16x16x32_bf16 v[66:69], v[192:195], v[224:227], v[66:69]
	s_setprio 0
	s_barrier
; #define PG8_STAGE(bufoff, gbase, voff) do { _Pragma("unroll") for (int _i = 0; _i < 2; ++_i) \
;         __builtin_amdgcn_global_load_lds((const unsigned*)((const char*)(gbase) + (voff)[_i]), (LAS unsigned*)(lds + (bufoff) + ldsw + _i * 8192), 16, 0, 0); } while (0)
; #define PG8_LDA(dst, b, h) do { if constexpr (FP8) { _Pragma("unroll") for (int m = 0; m < 4; ++m) dst##8[m] = PG8_LD8(lds + PG8_SA(b, h) + aoff + m * 2048); } \
;         else { _Pragma("unroll") for (int m = 0; m < 4; ++m) _Pragma("unroll") for (int k = 0; k < 2; ++k) dst[m][k] = *(const LAS bf16x8*)(lds + PG8_SA(b, h) + aoff + m * 2048 + k * 1024); } } while (0)
; #define PG8_WAIT_V(n) asm volatile("s_waitcnt vmcnt(" #n ")" ::: "memory")
; #define PG8_WAIT_L(n) asm volatile("s_waitcnt lgkmcnt(" #n ")" ::: "memory")
; #define PG8_BAR __builtin_amdgcn_s_barrier()
; #define PG8_SCHED __builtin_amdgcn_sched_barrier(0)
; template <class Epi, class Sched, bool ALIGN_EPI, bool SP2, bool FP8 = false>
; __device__ __forceinline__ void gemm_phase(LAS unsigned char* lds, const int K, const Sched& S, const Epi& E) {
;     ...
;             PG8_LDA(At, 1, 1); PG8_STAGE(PG8_SB(1, 0), b3, voffB); PG8_STAGE(PG8_SB(1, 1), b3 + hstep, voffB); PG8_STAGE(PG8_SA(1, 0), a3, vX0);
;             PG8_WAIT_V(8); PG8_WAIT_L(0); PG8_BAR; PG8_MMA(1, 0, At, B0); PG8_MMA(1, 1, At, B1); PG8_BAR; PG8_SCHED;
;         }
;         if constexpr (ALIGN_EPI) { if (wr == 0) PG8_BAR; }
	s_add_i32 s58, s69, s35
	v_lshl_add_u64 v[176:177], v[176:177], 0, s[38:39]
	s_mov_b32 m0, s58
	ds_read_b128 v[196:199], v184 offset:49152
	ds_read_b128 v[200:203], v184 offset:50176
	ds_read_b128 v[204:207], v184 offset:51200
	ds_read_b128 v[208:211], v184 offset:52224
	ds_read_b128 v[212:215], v184 offset:53248
	ds_read_b128 v[216:219], v184 offset:54272
	ds_read_b128 v[220:223], v184 offset:55296
	ds_read_b128 v[224:227], v184 offset:56320
	global_load_lds_dwordx4 v[176:177], off
	s_add_i32 m0, s58, 0x2000
	s_add_u32 s56, s56, 0x20080
	v_lshl_add_u64 v[176:177], v[228:229], 0, s[38:39]
	s_addc_u32 s57, s57, 0
	s_add_i32 s58, s70, s35
	global_load_lds_dwordx4 v[176:177], off
	v_lshl_add_u64 v[176:177], s[56:57], 0, v[154:155]
	s_mov_b32 m0, s58
	v_lshl_add_u64 v[152:153], v[152:153], 0, s[38:39]
	global_load_lds_dwordx4 v[176:177], off
	v_lshl_add_u64 v[176:177], s[56:57], 0, v[156:157]
	s_add_i32 m0, s58, 0x2000
	s_nop 0
	global_load_lds_dwordx4 v[176:177], off
	v_lshl_add_u64 v[176:177], v[230:231], 0, s[38:39]
	s_mov_b32 m0, s62
	s_nop 0
	global_load_lds_dwordx4 v[176:177], off
	s_mov_b32 m0, s63
	s_nop 0
	global_load_lds_dwordx4 v[152:153], off
	s_waitcnt vmcnt(8)
	s_waitcnt lgkmcnt(0)
	s_setprio 1
	s_barrier
	v_mfma_f32_16x16x32_bf16 v[62:65], v[140:143], v[196:199], v[62:65]
	v_mfma_f32_16x16x32_bf16 v[58:61], v[148:151], v[196:199], v[58:61]
	v_mfma_f32_16x16x32_bf16 v[46:49], v[140:143], v[204:207], v[46:49]
	v_mfma_f32_16x16x32_bf16 v[42:45], v[148:151], v[204:207], v[42:45]
	v_mfma_f32_16x16x32_bf16 v[22:25], v[140:143], v[212:215], v[22:25]
	v_mfma_f32_16x16x32_bf16 v[18:21], v[148:151], v[212:215], v[18:21]
	v_mfma_f32_16x16x32_bf16 v[6:9], v[140:143], v[220:223], v[6:9]
	v_mfma_f32_16x16x32_bf16 v[2:5], v[148:151], v[220:223], v[2:5]
	v_mfma_f32_16x16x32_bf16 v[62:65], v[144:147], v[200:203], v[62:65]
	v_mfma_f32_16x16x32_bf16 v[58:61], v[160:163], v[200:203], v[58:61]
	v_mfma_f32_16x16x32_bf16 v[46:49], v[144:147], v[208:211], v[46:49]
	v_mfma_f32_16x16x32_bf16 v[42:45], v[160:163], v[208:211], v[42:45]
	v_mfma_f32_16x16x32_bf16 v[22:25], v[144:147], v[216:219], v[22:25]
	v_mfma_f32_16x16x32_bf16 v[18:21], v[160:163], v[216:219], v[18:21]
	v_mfma_f32_16x16x32_bf16 v[6:9], v[144:147], v[224:227], v[6:9]
	v_mfma_f32_16x16x32_bf16 v[2:5], v[160:163], v[224:227], v[2:5]
	v_mfma_f32_16x16x32_bf16 v[54:57], v[164:167], v[196:199], v[54:57]
	v_mfma_f32_16x16x32_bf16 v[50:53], v[172:175], v[196:199], v[50:53]
	v_mfma_f32_16x16x32_bf16 v[38:41], v[164:167], v[204:207], v[38:41]
	v_mfma_f32_16x16x32_bf16 v[34:37], v[172:175], v[204:207], v[34:37]
	v_mfma_f32_16x16x32_bf16 v[30:33], v[164:167], v[212:215], v[30:33]
	v_mfma_f32_16x16x32_bf16 v[26:29], v[172:175], v[212:215], v[26:29]
	v_mfma_f32_16x16x32_bf16 v[14:17], v[164:167], v[220:223], v[14:17]
	v_mfma_f32_16x16x32_bf16 v[10:13], v[172:175], v[220:223], v[10:13]
	v_mfma_f32_16x16x32_bf16 v[54:57], v[168:171], v[200:203], v[54:57]
	v_mfma_f32_16x16x32_bf16 v[50:53], v[192:195], v[200:203], v[50:53]
	v_mfma_f32_16x16x32_bf16 v[38:41], v[168:171], v[208:211], v[38:41]
	v_mfma_f32_16x16x32_bf16 v[34:37], v[192:195], v[208:211], v[34:37]
	v_mfma_f32_16x16x32_bf16 v[30:33], v[168:171], v[216:219], v[30:33]
	v_mfma_f32_16x16x32_bf16 v[26:29], v[192:195], v[216:219], v[26:29]
	v_mfma_f32_16x16x32_bf16 v[14:17], v[168:171], v[224:227], v[14:17]
	v_mfma_f32_16x16x32_bf16 v[10:13], v[192:195], v[224:227], v[10:13]
	s_setprio 0
	s_barrier
	s_add_i32 s68, s68, 2
	s_add_u32 s50, s50, 0x100
	s_addc_u32 s51, s51, 0
	s_cmp_gt_u32 s68, 5
	s_cbranch_scc0 .LBB0_1025
	s_and_b64 vcc, exec, s[42:43]
	s_cbranch_vccz .LBB0_1028
	s_barrier

; #define PG8_STAGE(bufoff, gbase, voff) do { _Pragma("unroll") for (int _i = 0; _i < 2; ++_i) \
;         __builtin_amdgcn_global_load_lds((const unsigned*)((const char*)(gbase) + (voff)[_i]), (LAS unsigned*)(lds + (bufoff) + ldsw + _i * 8192), 16, 0, 0); } while (0)
; #define PG8_LDA(dst, b, h) do { if constexpr (FP8) { _Pragma("unroll") for (int m = 0; m < 4; ++m) dst##8[m] = PG8_LD8(lds + PG8_SA(b, h) + aoff + m * 2048); } \
;         else { _Pragma("unroll") for (int m = 0; m < 4; ++m) _Pragma("unroll") for (int k = 0; k < 2; ++k) dst[m][k] = *(const LAS bf16x8*)(lds + PG8_SA(b, h) + aoff + m * 2048 + k * 1024); } } while (0)
; #define PG8_LDB(dst, b, h) do { if constexpr (FP8) { _Pragma("unroll") for (int n = 0; n < 2; ++n) dst##8[n] = PG8_LD8(lds + PG8_SB(b, h) + boff + n * 2048); } \
;         else { _Pragma("unroll") for (int n = 0; n < 2; ++n) _Pragma("unroll") for (int k = 0; k < 2; ++k) dst[n][k] = *(const LAS bf16x8*)(lds + PG8_SB(b, h) + boff + n * 2048 + k * 1024); } } while (0)
; #define PG8_WAIT_V(n) asm volatile("s_waitcnt vmcnt(" #n ")" ::: "memory")
; #define PG8_WAIT_L(n) asm volatile("s_waitcnt lgkmcnt(" #n ")" ::: "memory")
; template <class Epi, class Sched, bool ALIGN_EPI, bool SP2, bool FP8 = false>
; __device__ __forceinline__ void gemm_phase(LAS unsigned char* lds, const int K, const Sched& S, const Epi& E) {
;     ...
;         for (int t = 0; t < nt; t += 2) {
;             const bool last = (t == nt - 2);
;             const char* a1 = cA + (size_t)(t + 1) * kstep;
;             const char* a2 = last ? nA : cA + (size_t)(t + 2) * kstep; const char* b2 = last ? nB : cB + (size_t)(t + 2) * kstep;
;             const char* a3 = a2 + kstep; const char* b3 = b2 + kstep;
;             unsigned vX0[2], vX1[2];
; #pragma unroll
;             for (int i = 0; i < 2; ++i) { vX0[i] = last ? vAn[0][i] : vAc[0][i]; vX1[i] = last ? vAn[1][i] : vAc[1][i]; }
;             PG8_LDB(B0, 0, 0); PG8_LDB(B1, 0, 1); PG8_SCHED; PG8_LDA(At, 0, 0); PG8_STAGE(PG8_SA(1, 1), a1, vAc[1]);
;             PG8_WAIT_V(8); PG8_WAIT_L(0); PG8_BAR; PG8_MMA(0, 0, At, B0); PG8_MMA(0, 1, At, B1); PG8_BAR; PG8_SCHED;
;             PG8_LDA(At, 0, 1); PG8_STAGE(PG8_SB(0, 0), b2, voffB); PG8_STAGE(PG8_SB(0, 1), b2 + hstep, voffB); PG8_STAGE(PG8_SA(0, 0), a2, vX0);
;             PG8_WAIT_V(8); PG8_WAIT_L(0); PG8_BAR; PG8_MMA(1, 0, At, B0); PG8_MMA(1, 1, At, B1); PG8_BAR; PG8_SCHED;
.LBB0_1189:
	s_add_u32 s49, s30, s50
	s_addc_u32 s56, s31, s51
	v_add_u32_e32 v2, s75, v193
	v_add_u32_e32 v14, s76, v193
	s_add_u32 s49, s49, 0x2c000100
	ds_read_b128 v[18:21], v2
	ds_read_b128 v[22:25], v2 offset:1024
	ds_read_b128 v[26:29], v2 offset:2048
	ds_read_b128 v[30:33], v2 offset:3072
	ds_read_b128 v[2:5], v14
	ds_read_b128 v[6:9], v14 offset:1024
	ds_read_b128 v[10:13], v14 offset:2048
	ds_read_b128 v[14:17], v14 offset:3072
	s_addc_u32 s58, s56, 0
	s_add_u32 s81, s43, s50
	s_addc_u32 s82, s45, s51
	s_cmpk_eq_i32 s50, 0x700
	s_cselect_b64 vcc, -1, 0
	s_and_b64 s[56:57], vcc, exec
	v_cndmask_b32_e32 v162, v211, v1, vcc
	s_cselect_b32 s59, s11, s58
	s_cselect_b32 s58, s10, s49
	v_cndmask_b32_e32 v171, v170, v189, vcc
	v_cndmask_b32_e32 v244, v174, v188, vcc
	v_cndmask_b32_e32 v173, v172, v191, vcc
	s_cselect_b32 s57, s41, s82
	s_cselect_b32 s56, s40, s81
	v_lshl_add_u64 v[236:237], v[178:179], 0, s[50:51]
	s_add_i32 m0, s64, 0xc000
	ds_read_b128 v[180:183], v204
	ds_read_b128 v[184:187], v204 offset:1024
	ds_read_b128 v[212:215], v204 offset:2048
	ds_read_b128 v[216:219], v204 offset:3072
	ds_read_b128 v[220:223], v204 offset:4096
	ds_read_b128 v[224:227], v204 offset:5120
	ds_read_b128 v[228:231], v204 offset:6144
	ds_read_b128 v[232:235], v204 offset:7168
	global_load_lds_dwordx4 v[236:237], off
	v_lshl_add_u64 v[236:237], v[176:177], 0, s[50:51]
	s_add_i32 m0, s64, 0xe000
	s_nop 0
	global_load_lds_dwordx4 v[236:237], off
	s_waitcnt vmcnt(8)
	s_waitcnt lgkmcnt(0)
	s_setprio 1
	s_barrier
	v_mfma_f32_16x16x128_f8f6f4 v[150:153], v[18:25], v[180:187], v[150:153]
	v_mfma_f32_16x16x128_f8f6f4 v[158:161], v[26:33], v[180:187], v[158:161]
	v_mfma_f32_16x16x128_f8f6f4 v[134:137], v[18:25], v[212:219], v[134:137]
	v_mfma_f32_16x16x128_f8f6f4 v[142:145], v[26:33], v[212:219], v[142:145]
	v_mfma_f32_16x16x128_f8f6f4 v[118:121], v[18:25], v[220:227], v[118:121]
	v_mfma_f32_16x16x128_f8f6f4 v[126:129], v[26:33], v[220:227], v[126:129]
	v_mfma_f32_16x16x128_f8f6f4 v[102:105], v[18:25], v[228:235], v[102:105]
	v_mfma_f32_16x16x128_f8f6f4 v[110:113], v[26:33], v[228:235], v[110:113]
	v_mfma_f32_16x16x128_f8f6f4 v[146:149], v[2:9], v[180:187], v[146:149]
	v_mfma_f32_16x16x128_f8f6f4 v[154:157], v[10:17], v[180:187], v[154:157]
	v_mfma_f32_16x16x128_f8f6f4 v[130:133], v[2:9], v[212:219], v[130:133]
	v_mfma_f32_16x16x128_f8f6f4 v[138:141], v[10:17], v[212:219], v[138:141]
	v_mfma_f32_16x16x128_f8f6f4 v[114:117], v[2:9], v[220:227], v[114:117]
	v_mfma_f32_16x16x128_f8f6f4 v[122:125], v[10:17], v[220:227], v[122:125]
	v_mfma_f32_16x16x128_f8f6f4 v[98:101], v[2:9], v[228:235], v[98:101]
	v_mfma_f32_16x16x128_f8f6f4 v[106:109], v[10:17], v[228:235], v[106:109]
	s_setprio 0
	s_barrier
	s_add_i32 s49, s75, s63
	v_lshl_add_u64 v[180:181], s[56:57], 0, v[164:165]
	s_mov_b32 m0, s49
	ds_read_b128 v[212:215], v204 offset:16384
	ds_read_b128 v[216:219], v204 offset:17408
	ds_read_b128 v[220:223], v204 offset:18432
	ds_read_b128 v[224:227], v204 offset:19456
	ds_read_b128 v[228:231], v204 offset:20480
	ds_read_b128 v[232:235], v204 offset:21504
	ds_read_b128 v[236:239], v204 offset:22528
	ds_read_b128 v[240:243], v204 offset:23552
	global_load_lds_dwordx4 v[180:181], off
	s_add_i32 m0, s49, 0x2000
	s_add_u32 s82, s56, 0x40000
	v_lshl_add_u64 v[182:183], s[56:57], 0, v[166:167]
	s_addc_u32 s83, s57, 0
	s_add_i32 s49, s76, s63
	global_load_lds_dwordx4 v[182:183], off
	v_lshl_add_u64 v[184:185], s[82:83], 0, v[164:165]
	s_mov_b32 m0, s49
	v_mov_b32_e32 v245, v163
	global_load_lds_dwordx4 v[184:185], off
	v_lshl_add_u64 v[184:185], s[82:83], 0, v[166:167]
	s_add_i32 m0, s49, 0x2000
	v_lshl_add_u64 v[186:187], s[58:59], 0, v[162:163]
	global_load_lds_dwordx4 v[184:185], off
	s_mov_b32 m0, s64
	v_lshl_add_u64 v[184:185], s[58:59], 0, v[244:245]
	global_load_lds_dwordx4 v162, s[58:59]
	s_mov_b32 m0, s65
	s_nop 0
	global_load_lds_dwordx4 v244, s[58:59]
	s_waitcnt vmcnt(8)
	s_waitcnt lgkmcnt(0)
	s_setprio 1
	s_barrier
	v_mfma_f32_16x16x128_f8f6f4 v[86:89], v[18:25], v[212:219], v[86:89]
	v_mfma_f32_16x16x128_f8f6f4 v[94:97], v[26:33], v[212:219], v[94:97]
	v_mfma_f32_16x16x128_f8f6f4 v[66:69], v[18:25], v[220:227], v[66:69]
	v_mfma_f32_16x16x128_f8f6f4 v[78:81], v[26:33], v[220:227], v[78:81]
	v_mfma_f32_16x16x128_f8f6f4 v[46:49], v[18:25], v[228:235], v[46:49]
	v_mfma_f32_16x16x128_f8f6f4 v[54:57], v[26:33], v[228:235], v[54:57]
	v_mfma_f32_16x16x128_f8f6f4 v[34:37], v[18:25], v[236:243], v[34:37]
	v_mfma_f32_16x16x128_f8f6f4 v[38:41], v[26:33], v[236:243], v[38:41]
	v_mfma_f32_16x16x128_f8f6f4 v[82:85], v[2:9], v[212:219], v[82:85]
	v_mfma_f32_16x16x128_f8f6f4 v[90:93], v[10:17], v[212:219], v[90:93]
	v_mfma_f32_16x16x128_f8f6f4 v[62:65], v[2:9], v[220:227], v[62:65]
	v_mfma_f32_16x16x128_f8f6f4 v[74:77], v[10:17], v[220:227], v[74:77]
	v_mfma_f32_16x16x128_f8f6f4 v[58:61], v[2:9], v[228:235], v[58:61]
	v_mfma_f32_16x16x128_f8f6f4 v[70:73], v[10:17], v[228:235], v[70:73]
	v_mfma_f32_16x16x128_f8f6f4 v[42:45], v[2:9], v[236:243], v[42:45]
	v_mfma_f32_16x16x128_f8f6f4 v[50:53], v[10:17], v[236:243], v[50:53]
	s_setprio 0
	s_barrier
; #define PG8_STAGE(bufoff, gbase, voff) do { _Pragma("unroll") for (int _i = 0; _i < 2; ++_i) \
;         __builtin_amdgcn_global_load_lds((const unsigned*)((const char*)(gbase) + (voff)[_i]), (LAS unsigned*)(lds + (bufoff) + ldsw + _i * 8192), 16, 0, 0); } while (0)
; #define PG8_LDA(dst, b, h) do { if constexpr (FP8) { _Pragma("unroll") for (int m = 0; m < 4; ++m) dst##8[m] = PG8_LD8(lds + PG8_SA(b, h) + aoff + m * 2048); } \
;         else { _Pragma("unroll") for (int m = 0; m < 4; ++m) _Pragma("unroll") for (int k = 0; k < 2; ++k) dst[m][k] = *(const LAS bf16x8*)(lds + PG8_SA(b, h) + aoff + m * 2048 + k * 1024); } } while (0)
; #define PG8_LDB(dst, b, h) do { if constexpr (FP8) { _Pragma("unroll") for (int n = 0; n < 2; ++n) dst##8[n] = PG8_LD8(lds + PG8_SB(b, h) + boff + n * 2048); } \
;         else { _Pragma("unroll") for (int n = 0; n < 2; ++n) _Pragma("unroll") for (int k = 0; k < 2; ++k) dst[n][k] = *(const LAS bf16x8*)(lds + PG8_SB(b, h) + boff + n * 2048 + k * 1024); } } while (0)
; #define PG8_WAIT_V(n) asm volatile("s_waitcnt vmcnt(" #n ")" ::: "memory")
; #define PG8_WAIT_L(n) asm volatile("s_waitcnt lgkmcnt(" #n ")" ::: "memory")
; #define PG8_BAR __builtin_amdgcn_s_barrier()
; #define PG8_SCHED __builtin_amdgcn_sched_barrier(0)
; template <class Epi, class Sched, bool ALIGN_EPI, bool SP2, bool FP8 = false>
; __device__ __forceinline__ void gemm_phase(LAS unsigned char* lds, const int K, const Sched& S, const Epi& E) {
;     ...
;             PG8_LDB(B0, 1, 0); PG8_LDB(B1, 1, 1); PG8_SCHED; PG8_LDA(At, 1, 0); PG8_STAGE(PG8_SA(0, 1), a2, vX1);
;             PG8_WAIT_V(8); PG8_WAIT_L(0); PG8_BAR; PG8_MMA(0, 0, At, B0); PG8_MMA(0, 1, At, B1); PG8_BAR; PG8_SCHED;
;             PG8_LDA(At, 1, 1); PG8_STAGE(PG8_SB(1, 0), b3, voffB); PG8_STAGE(PG8_SB(1, 1), b3 + hstep, voffB); PG8_STAGE(PG8_SA(1, 0), a3, vX0);
;             PG8_WAIT_V(8); PG8_WAIT_L(0); PG8_BAR; PG8_MMA(1, 0, At, B0); PG8_MMA(1, 1, At, B1); PG8_BAR; PG8_SCHED;
;         }
;         if constexpr (ALIGN_EPI) { if (wr == 0) PG8_BAR; }
	s_add_i32 s49, 0, 0x18000
	s_add_i32 s81, 0, 0x1c000
	v_add_u32_e32 v14, s49, v193
	v_add_u32_e32 v30, s81, v193
	ds_read_b128 v[2:5], v14
	ds_read_b128 v[6:9], v14 offset:1024
	ds_read_b128 v[10:13], v14 offset:2048
	ds_read_b128 v[14:17], v14 offset:3072
	ds_read_b128 v[18:21], v30
	ds_read_b128 v[22:25], v30 offset:1024
	ds_read_b128 v[26:29], v30 offset:2048
	ds_read_b128 v[30:33], v30 offset:3072
	s_mov_b32 m0, s66
	ds_read_b128 v[212:215], v204 offset:32768
	ds_read_b128 v[216:219], v204 offset:33792
	ds_read_b128 v[220:223], v204 offset:34816
	ds_read_b128 v[224:227], v204 offset:35840
	ds_read_b128 v[228:231], v204 offset:36864
	ds_read_b128 v[232:235], v204 offset:37888
	ds_read_b128 v[236:239], v204 offset:38912
	ds_read_b128 v[240:243], v204 offset:39936
	global_load_lds_dwordx4 v171, s[58:59]
	s_mov_b32 m0, s67
	s_nop 0
	global_load_lds_dwordx4 v173, s[58:59]
	s_waitcnt vmcnt(8)
	s_waitcnt lgkmcnt(0)
	s_setprio 1
	s_barrier
	v_mfma_f32_16x16x128_f8f6f4 v[150:153], v[2:9], v[212:219], v[150:153]
	v_mfma_f32_16x16x128_f8f6f4 v[158:161], v[10:17], v[212:219], v[158:161]
	v_mfma_f32_16x16x128_f8f6f4 v[134:137], v[2:9], v[220:227], v[134:137]
	v_mfma_f32_16x16x128_f8f6f4 v[142:145], v[10:17], v[220:227], v[142:145]
	v_mfma_f32_16x16x128_f8f6f4 v[118:121], v[2:9], v[228:235], v[118:121]
	v_mfma_f32_16x16x128_f8f6f4 v[126:129], v[10:17], v[228:235], v[126:129]
	v_mfma_f32_16x16x128_f8f6f4 v[102:105], v[2:9], v[236:243], v[102:105]
	v_mfma_f32_16x16x128_f8f6f4 v[110:113], v[10:17], v[236:243], v[110:113]
	v_mfma_f32_16x16x128_f8f6f4 v[146:149], v[18:25], v[212:219], v[146:149]
	v_mfma_f32_16x16x128_f8f6f4 v[154:157], v[26:33], v[212:219], v[154:157]
	v_mfma_f32_16x16x128_f8f6f4 v[130:133], v[18:25], v[220:227], v[130:133]
	v_mfma_f32_16x16x128_f8f6f4 v[138:141], v[26:33], v[220:227], v[138:141]
	v_mfma_f32_16x16x128_f8f6f4 v[114:117], v[18:25], v[228:235], v[114:117]
	v_mfma_f32_16x16x128_f8f6f4 v[122:125], v[26:33], v[228:235], v[122:125]
	v_mfma_f32_16x16x128_f8f6f4 v[98:101], v[18:25], v[236:243], v[98:101]
	v_mfma_f32_16x16x128_f8f6f4 v[106:109], v[26:33], v[236:243], v[106:109]
	s_setprio 0
	s_barrier
	s_add_i32 s49, s49, s63
	v_lshl_add_u64 v[180:181], v[180:181], 0, s[16:17]
	s_mov_b32 m0, s49
	ds_read_b128 v[212:215], v204 offset:49152
	ds_read_b128 v[216:219], v204 offset:50176
	ds_read_b128 v[220:223], v204 offset:51200
	ds_read_b128 v[224:227], v204 offset:52224
	ds_read_b128 v[228:231], v204 offset:53248
	ds_read_b128 v[232:235], v204 offset:54272
	ds_read_b128 v[236:239], v204 offset:55296
	ds_read_b128 v[240:243], v204 offset:56320
	global_load_lds_dwordx4 v[180:181], off
	s_add_i32 m0, s49, 0x2000
	s_add_u32 s56, s56, 0x40080
	v_lshl_add_u64 v[180:181], v[182:183], 0, s[16:17]
	s_addc_u32 s57, s57, 0
	s_add_i32 s49, s81, s63
	global_load_lds_dwordx4 v[180:181], off
	v_lshl_add_u64 v[180:181], s[56:57], 0, v[164:165]
	s_mov_b32 m0, s49
	s_nop 0
	global_load_lds_dwordx4 v[180:181], off
	v_lshl_add_u64 v[180:181], s[56:57], 0, v[166:167]
	s_add_i32 m0, s49, 0x2000
	s_nop 0
	global_load_lds_dwordx4 v[180:181], off
	v_lshl_add_u64 v[180:181], v[186:187], 0, s[16:17]
	s_mov_b32 m0, s70
	s_nop 0
	global_load_lds_dwordx4 v[180:181], off
	v_lshl_add_u64 v[180:181], v[184:185], 0, s[16:17]
	s_mov_b32 m0, s71
	s_nop 0
	global_load_lds_dwordx4 v[180:181], off
	s_waitcnt vmcnt(8)
	s_waitcnt lgkmcnt(0)
	s_setprio 1
	s_barrier
	v_mfma_f32_16x16x128_f8f6f4 v[86:89], v[2:9], v[212:219], v[86:89]
	v_mfma_f32_16x16x128_f8f6f4 v[94:97], v[10:17], v[212:219], v[94:97]
	v_mfma_f32_16x16x128_f8f6f4 v[66:69], v[2:9], v[220:227], v[66:69]
	v_mfma_f32_16x16x128_f8f6f4 v[78:81], v[10:17], v[220:227], v[78:81]
	v_mfma_f32_16x16x128_f8f6f4 v[46:49], v[2:9], v[228:235], v[46:49]
	v_mfma_f32_16x16x128_f8f6f4 v[54:57], v[10:17], v[228:235], v[54:57]
	v_mfma_f32_16x16x128_f8f6f4 v[34:37], v[2:9], v[236:243], v[34:37]
	v_mfma_f32_16x16x128_f8f6f4 v[38:41], v[10:17], v[236:243], v[38:41]
	v_mfma_f32_16x16x128_f8f6f4 v[82:85], v[18:25], v[212:219], v[82:85]
	v_mfma_f32_16x16x128_f8f6f4 v[90:93], v[26:33], v[212:219], v[90:93]
	v_mfma_f32_16x16x128_f8f6f4 v[62:65], v[18:25], v[220:227], v[62:65]
	v_mfma_f32_16x16x128_f8f6f4 v[74:77], v[26:33], v[220:227], v[74:77]
	v_mfma_f32_16x16x128_f8f6f4 v[58:61], v[18:25], v[228:235], v[58:61]
	v_mfma_f32_16x16x128_f8f6f4 v[70:73], v[26:33], v[228:235], v[70:73]
	v_mfma_f32_16x16x128_f8f6f4 v[42:45], v[18:25], v[236:243], v[42:45]
	v_mfma_f32_16x16x128_f8f6f4 v[50:53], v[26:33], v[236:243], v[50:53]
	s_setprio 0
	s_barrier
	s_add_i32 s47, s47, 2
	s_add_u32 s50, s50, 0x100
	s_addc_u32 s51, s51, 0
	s_cmp_gt_u32 s47, 13
	s_cbranch_scc0 .LBB0_1189
	s_and_b64 vcc, exec, s[38:39]
	s_cbranch_vccz .LBB0_1192
	s_barrier

; #define PG8_STAGE(bufoff, gbase, voff) do { _Pragma("unroll") for (int _i = 0; _i < 2; ++_i) \
;         __builtin_amdgcn_global_load_lds((const unsigned*)((const char*)(gbase) + (voff)[_i]), (LAS unsigned*)(lds + (bufoff) + ldsw + _i * 8192), 16, 0, 0); } while (0)
; #define PG8_LDA(dst, b, h) do { if constexpr (FP8) { _Pragma("unroll") for (int m = 0; m < 4; ++m) dst##8[m] = PG8_LD8(lds + PG8_SA(b, h) + aoff + m * 2048); } \
;         else { _Pragma("unroll") for (int m = 0; m < 4; ++m) _Pragma("unroll") for (int k = 0; k < 2; ++k) dst[m][k] = *(const LAS bf16x8*)(lds + PG8_SA(b, h) + aoff + m * 2048 + k * 1024); } } while (0)
; #define PG8_LDB(dst, b, h) do { if constexpr (FP8) { _Pragma("unroll") for (int n = 0; n < 2; ++n) dst##8[n] = PG8_LD8(lds + PG8_SB(b, h) + boff + n * 2048); } \
;         else { _Pragma("unroll") for (int n = 0; n < 2; ++n) _Pragma("unroll") for (int k = 0; k < 2; ++k) dst[n][k] = *(const LAS bf16x8*)(lds + PG8_SB(b, h) + boff + n * 2048 + k * 1024); } } while (0)
; #define PG8_WAIT_V(n) asm volatile("s_waitcnt vmcnt(" #n ")" ::: "memory")
; #define PG8_WAIT_L(n) asm volatile("s_waitcnt lgkmcnt(" #n ")" ::: "memory")
; template <class Epi, class Sched, bool ALIGN_EPI, bool SP2, bool FP8 = false>
; __device__ __forceinline__ void gemm_phase(LAS unsigned char* lds, const int K, const Sched& S, const Epi& E) {
;     ...
;         for (int t = 0; t < nt; t += 2) {
;             const bool last = (t == nt - 2);
;             const char* a1 = cA + (size_t)(t + 1) * kstep;
;             const char* a2 = last ? nA : cA + (size_t)(t + 2) * kstep; const char* b2 = last ? nB : cB + (size_t)(t + 2) * kstep;
;             const char* a3 = a2 + kstep; const char* b3 = b2 + kstep;
;             unsigned vX0[2], vX1[2];
; #pragma unroll
;             for (int i = 0; i < 2; ++i) { vX0[i] = last ? vAn[0][i] : vAc[0][i]; vX1[i] = last ? vAn[1][i] : vAc[1][i]; }
;             PG8_LDB(B0, 0, 0); PG8_LDB(B1, 0, 1); PG8_SCHED; PG8_LDA(At, 0, 0); PG8_STAGE(PG8_SA(1, 1), a1, vAc[1]);
;             PG8_WAIT_V(8); PG8_WAIT_L(0); PG8_BAR; PG8_MMA(0, 0, At, B0); PG8_MMA(0, 1, At, B1); PG8_BAR; PG8_SCHED;
;             PG8_LDA(At, 0, 1); PG8_STAGE(PG8_SB(0, 0), b2, voffB); PG8_STAGE(PG8_SB(0, 1), b2 + hstep, voffB); PG8_STAGE(PG8_SA(0, 0), a2, vX0);
;             PG8_WAIT_V(8); PG8_WAIT_L(0); PG8_BAR; PG8_MMA(1, 0, At, B0); PG8_MMA(1, 1, At, B1); PG8_BAR; PG8_SCHED;
.LBB0_1329:
	s_add_u32 s56, s30, s50
	s_addc_u32 s57, s31, s51
	s_add_u32 s58, s56, 0x60000100
	s_addc_u32 s59, s57, 0
	s_add_u32 s81, s41, s50
	s_addc_u32 s82, s43, s51
	s_cmpk_eq_i32 s50, 0x700
	s_cselect_b64 vcc, -1, 0
	s_and_b64 s[56:57], vcc, exec
	s_cselect_b32 s59, s9, s59
	s_cselect_b32 s58, s8, s58
	s_cselect_b32 s57, s45, s82
	s_cselect_b32 s56, s44, s81
	s_add_i32 s81, 0, 0x10000
	s_add_i32 s82, 0, 0x14000
	v_add_u32_e32 v2, s81, v196
	v_add_u32_e32 v14, s82, v196
	ds_read_b128 v[18:21], v2
	ds_read_b128 v[22:25], v2 offset:1024
	ds_read_b128 v[26:29], v2 offset:2048
	ds_read_b128 v[30:33], v2 offset:3072
	ds_read_b128 v[2:5], v14
	ds_read_b128 v[6:9], v14 offset:1024
	ds_read_b128 v[10:13], v14 offset:2048
	ds_read_b128 v[14:17], v14 offset:3072
	v_cndmask_b32_e32 v166, v172, v204, vcc
	v_cndmask_b32_e32 v171, v170, v205, vcc
	v_cndmask_b32_e32 v240, v176, v206, vcc
	v_cndmask_b32_e32 v175, v174, v207, vcc
	v_lshl_add_u64 v[232:233], v[180:181], 0, s[50:51]
	s_add_i32 m0, s71, 0xc000
	ds_read_b128 v[182:185], v203
	ds_read_b128 v[186:189], v203 offset:1024
	ds_read_b128 v[208:211], v203 offset:2048
	ds_read_b128 v[212:215], v203 offset:3072
	ds_read_b128 v[216:219], v203 offset:4096
	ds_read_b128 v[220:223], v203 offset:5120
	ds_read_b128 v[224:227], v203 offset:6144
	ds_read_b128 v[228:231], v203 offset:7168
	global_load_lds_dwordx4 v[232:233], off
	v_lshl_add_u64 v[232:233], v[178:179], 0, s[50:51]
	s_add_i32 m0, s71, 0xe000
	s_nop 0
	global_load_lds_dwordx4 v[232:233], off
	s_waitcnt vmcnt(8)
	s_waitcnt lgkmcnt(0)
	s_setprio 1
	s_barrier
	v_mfma_f32_16x16x128_f8f6f4 v[158:161], v[18:25], v[182:189], v[158:161]
	v_mfma_f32_16x16x128_f8f6f4 v[154:157], v[26:33], v[182:189], v[154:157]
	v_mfma_f32_16x16x128_f8f6f4 v[142:145], v[18:25], v[208:215], v[142:145]
	v_mfma_f32_16x16x128_f8f6f4 v[138:141], v[26:33], v[208:215], v[138:141]
	v_mfma_f32_16x16x128_f8f6f4 v[126:129], v[18:25], v[216:223], v[126:129]
	v_mfma_f32_16x16x128_f8f6f4 v[122:125], v[26:33], v[216:223], v[122:125]
	v_mfma_f32_16x16x128_f8f6f4 v[110:113], v[18:25], v[224:231], v[110:113]
	v_mfma_f32_16x16x128_f8f6f4 v[106:109], v[26:33], v[224:231], v[106:109]
	v_mfma_f32_16x16x128_f8f6f4 v[150:153], v[2:9], v[182:189], v[150:153]
	v_mfma_f32_16x16x128_f8f6f4 v[146:149], v[10:17], v[182:189], v[146:149]
	v_mfma_f32_16x16x128_f8f6f4 v[134:137], v[2:9], v[208:215], v[134:137]
	v_mfma_f32_16x16x128_f8f6f4 v[130:133], v[10:17], v[208:215], v[130:133]
	v_mfma_f32_16x16x128_f8f6f4 v[118:121], v[2:9], v[216:223], v[118:121]
	v_mfma_f32_16x16x128_f8f6f4 v[114:117], v[10:17], v[216:223], v[114:117]
	v_mfma_f32_16x16x128_f8f6f4 v[102:105], v[2:9], v[224:231], v[102:105]
	v_mfma_f32_16x16x128_f8f6f4 v[98:101], v[10:17], v[224:231], v[98:101]
	s_setprio 0
	s_barrier
	s_add_i32 s81, s81, s70
	v_lshl_add_u64 v[182:183], s[56:57], 0, v[162:163]
	s_mov_b32 m0, s81
	ds_read_b128 v[208:211], v203 offset:16384
	ds_read_b128 v[212:215], v203 offset:17408
	ds_read_b128 v[216:219], v203 offset:18432
	ds_read_b128 v[220:223], v203 offset:19456
	ds_read_b128 v[224:227], v203 offset:20480
	ds_read_b128 v[228:231], v203 offset:21504
	ds_read_b128 v[232:235], v203 offset:22528
	ds_read_b128 v[236:239], v203 offset:23552
	global_load_lds_dwordx4 v[182:183], off
	s_add_i32 m0, s81, 0x2000
	s_add_u32 s84, s56, 0x40000
	v_lshl_add_u64 v[184:185], s[56:57], 0, v[164:165]
	s_addc_u32 s85, s57, 0
	s_add_i32 s81, s82, s70
	global_load_lds_dwordx4 v[184:185], off
	v_lshl_add_u64 v[186:187], s[84:85], 0, v[162:163]
	s_mov_b32 m0, s81
	v_mov_b32_e32 v241, v167
	global_load_lds_dwordx4 v[186:187], off
	v_lshl_add_u64 v[186:187], s[84:85], 0, v[164:165]
	s_add_i32 m0, s81, 0x2000
	v_lshl_add_u64 v[188:189], s[58:59], 0, v[166:167]
	global_load_lds_dwordx4 v[186:187], off
	s_mov_b32 m0, s71
	v_lshl_add_u64 v[186:187], s[58:59], 0, v[240:241]
	global_load_lds_dwordx4 v166, s[58:59]
	s_mov_b32 m0, s72
	s_nop 0
	global_load_lds_dwordx4 v240, s[58:59]
	s_waitcnt vmcnt(8)
	s_waitcnt lgkmcnt(0)
	s_setprio 1
	s_barrier
	v_mfma_f32_16x16x128_f8f6f4 v[94:97], v[18:25], v[208:215], v[94:97]
	v_mfma_f32_16x16x128_f8f6f4 v[90:93], v[26:33], v[208:215], v[90:93]
	v_mfma_f32_16x16x128_f8f6f4 v[78:81], v[18:25], v[216:223], v[78:81]
	v_mfma_f32_16x16x128_f8f6f4 v[74:77], v[26:33], v[216:223], v[74:77]
	v_mfma_f32_16x16x128_f8f6f4 v[58:61], v[18:25], v[224:231], v[58:61]
	v_mfma_f32_16x16x128_f8f6f4 v[46:49], v[26:33], v[224:231], v[46:49]
	v_mfma_f32_16x16x128_f8f6f4 v[38:41], v[18:25], v[232:239], v[38:41]
	v_mfma_f32_16x16x128_f8f6f4 v[34:37], v[26:33], v[232:239], v[34:37]
	v_mfma_f32_16x16x128_f8f6f4 v[86:89], v[2:9], v[208:215], v[86:89]
	v_mfma_f32_16x16x128_f8f6f4 v[82:85], v[10:17], v[208:215], v[82:85]
	v_mfma_f32_16x16x128_f8f6f4 v[62:65], v[2:9], v[216:223], v[62:65]
	v_mfma_f32_16x16x128_f8f6f4 v[54:57], v[10:17], v[216:223], v[54:57]
	v_mfma_f32_16x16x128_f8f6f4 v[70:73], v[2:9], v[224:231], v[70:73]
	v_mfma_f32_16x16x128_f8f6f4 v[66:69], v[10:17], v[224:231], v[66:69]
	v_mfma_f32_16x16x128_f8f6f4 v[50:53], v[2:9], v[232:239], v[50:53]
	v_mfma_f32_16x16x128_f8f6f4 v[42:45], v[10:17], v[232:239], v[42:45]
	s_setprio 0
	s_barrier
; #define PG8_STAGE(bufoff, gbase, voff) do { _Pragma("unroll") for (int _i = 0; _i < 2; ++_i) \
;         __builtin_amdgcn_global_load_lds((const unsigned*)((const char*)(gbase) + (voff)[_i]), (LAS unsigned*)(lds + (bufoff) + ldsw + _i * 8192), 16, 0, 0); } while (0)
; #define PG8_LDA(dst, b, h) do { if constexpr (FP8) { _Pragma("unroll") for (int m = 0; m < 4; ++m) dst##8[m] = PG8_LD8(lds + PG8_SA(b, h) + aoff + m * 2048); } \
;         else { _Pragma("unroll") for (int m = 0; m < 4; ++m) _Pragma("unroll") for (int k = 0; k < 2; ++k) dst[m][k] = *(const LAS bf16x8*)(lds + PG8_SA(b, h) + aoff + m * 2048 + k * 1024); } } while (0)
; #define PG8_LDB(dst, b, h) do { if constexpr (FP8) { _Pragma("unroll") for (int n = 0; n < 2; ++n) dst##8[n] = PG8_LD8(lds + PG8_SB(b, h) + boff + n * 2048); } \
;         else { _Pragma("unroll") for (int n = 0; n < 2; ++n) _Pragma("unroll") for (int k = 0; k < 2; ++k) dst[n][k] = *(const LAS bf16x8*)(lds + PG8_SB(b, h) + boff + n * 2048 + k * 1024); } } while (0)
; #define PG8_WAIT_V(n) asm volatile("s_waitcnt vmcnt(" #n ")" ::: "memory")
; #define PG8_WAIT_L(n) asm volatile("s_waitcnt lgkmcnt(" #n ")" ::: "memory")
; #define PG8_BAR __builtin_amdgcn_s_barrier()
; #define PG8_SCHED __builtin_amdgcn_sched_barrier(0)
; template <class Epi, class Sched, bool ALIGN_EPI, bool SP2, bool FP8 = false>
; __device__ __forceinline__ void gemm_phase(LAS unsigned char* lds, const int K, const Sched& S, const Epi& E) {
;     ...
;             PG8_LDB(B0, 1, 0); PG8_LDB(B1, 1, 1); PG8_SCHED; PG8_LDA(At, 1, 0); PG8_STAGE(PG8_SA(0, 1), a2, vX1);
;             PG8_WAIT_V(8); PG8_WAIT_L(0); PG8_BAR; PG8_MMA(0, 0, At, B0); PG8_MMA(0, 1, At, B1); PG8_BAR; PG8_SCHED;
;             PG8_LDA(At, 1, 1); PG8_STAGE(PG8_SB(1, 0), b3, voffB); PG8_STAGE(PG8_SB(1, 1), b3 + hstep, voffB); PG8_STAGE(PG8_SA(1, 0), a3, vX0);
;             PG8_WAIT_V(8); PG8_WAIT_L(0); PG8_BAR; PG8_MMA(1, 0, At, B0); PG8_MMA(1, 1, At, B1); PG8_BAR; PG8_SCHED;
;         }
;         if constexpr (ALIGN_EPI) { if (wr == 0) PG8_BAR; }
	s_add_i32 s81, 0, 0x18000
	s_add_i32 s82, 0, 0x1c000
	v_add_u32_e32 v14, s81, v196
	v_add_u32_e32 v30, s82, v196
	ds_read_b128 v[2:5], v14
	ds_read_b128 v[6:9], v14 offset:1024
	ds_read_b128 v[10:13], v14 offset:2048
	ds_read_b128 v[14:17], v14 offset:3072
	ds_read_b128 v[18:21], v30
	ds_read_b128 v[22:25], v30 offset:1024
	ds_read_b128 v[26:29], v30 offset:2048
	ds_read_b128 v[30:33], v30 offset:3072
	s_mov_b32 m0, s73
	ds_read_b128 v[208:211], v203 offset:32768
	ds_read_b128 v[212:215], v203 offset:33792
	ds_read_b128 v[216:219], v203 offset:34816
	ds_read_b128 v[220:223], v203 offset:35840
	ds_read_b128 v[224:227], v203 offset:36864
	ds_read_b128 v[228:231], v203 offset:37888
	ds_read_b128 v[232:235], v203 offset:38912
	ds_read_b128 v[236:239], v203 offset:39936
	global_load_lds_dwordx4 v171, s[58:59]
	s_mov_b32 m0, s74
	s_nop 0
	global_load_lds_dwordx4 v175, s[58:59]
	s_waitcnt vmcnt(8)
	s_waitcnt lgkmcnt(0)
	s_setprio 1
	s_barrier
	v_mfma_f32_16x16x128_f8f6f4 v[158:161], v[2:9], v[208:215], v[158:161]
	v_mfma_f32_16x16x128_f8f6f4 v[154:157], v[10:17], v[208:215], v[154:157]
	v_mfma_f32_16x16x128_f8f6f4 v[142:145], v[2:9], v[216:223], v[142:145]
	v_mfma_f32_16x16x128_f8f6f4 v[138:141], v[10:17], v[216:223], v[138:141]
	v_mfma_f32_16x16x128_f8f6f4 v[126:129], v[2:9], v[224:231], v[126:129]
	v_mfma_f32_16x16x128_f8f6f4 v[122:125], v[10:17], v[224:231], v[122:125]
	v_mfma_f32_16x16x128_f8f6f4 v[110:113], v[2:9], v[232:239], v[110:113]
	v_mfma_f32_16x16x128_f8f6f4 v[106:109], v[10:17], v[232:239], v[106:109]
	v_mfma_f32_16x16x128_f8f6f4 v[150:153], v[18:25], v[208:215], v[150:153]
	v_mfma_f32_16x16x128_f8f6f4 v[146:149], v[26:33], v[208:215], v[146:149]
	v_mfma_f32_16x16x128_f8f6f4 v[134:137], v[18:25], v[216:223], v[134:137]
	v_mfma_f32_16x16x128_f8f6f4 v[130:133], v[26:33], v[216:223], v[130:133]
	v_mfma_f32_16x16x128_f8f6f4 v[118:121], v[18:25], v[224:231], v[118:121]
	v_mfma_f32_16x16x128_f8f6f4 v[114:117], v[26:33], v[224:231], v[114:117]
	v_mfma_f32_16x16x128_f8f6f4 v[102:105], v[18:25], v[232:239], v[102:105]
	v_mfma_f32_16x16x128_f8f6f4 v[98:101], v[26:33], v[232:239], v[98:101]
	s_setprio 0
	s_barrier
	s_add_i32 s58, s81, s70
	v_lshl_add_u64 v[182:183], v[182:183], 0, s[18:19]
	s_mov_b32 m0, s58
	ds_read_b128 v[208:211], v203 offset:49152
	ds_read_b128 v[212:215], v203 offset:50176
	ds_read_b128 v[216:219], v203 offset:51200
	ds_read_b128 v[220:223], v203 offset:52224
	ds_read_b128 v[224:227], v203 offset:53248
	ds_read_b128 v[228:231], v203 offset:54272
	ds_read_b128 v[232:235], v203 offset:55296
	ds_read_b128 v[236:239], v203 offset:56320
	global_load_lds_dwordx4 v[182:183], off
	s_add_i32 m0, s58, 0x2000
	s_add_u32 s56, s56, 0x40080
	v_lshl_add_u64 v[182:183], v[184:185], 0, s[18:19]
	s_addc_u32 s57, s57, 0
	s_add_i32 s58, s82, s70
	global_load_lds_dwordx4 v[182:183], off
	v_lshl_add_u64 v[182:183], s[56:57], 0, v[162:163]
	s_mov_b32 m0, s58
	s_nop 0
	global_load_lds_dwordx4 v[182:183], off
	v_lshl_add_u64 v[182:183], s[56:57], 0, v[164:165]
	s_add_i32 m0, s58, 0x2000
	s_nop 0
	global_load_lds_dwordx4 v[182:183], off
	v_lshl_add_u64 v[182:183], v[188:189], 0, s[18:19]
	s_mov_b32 m0, s75
	s_nop 0
	global_load_lds_dwordx4 v[182:183], off
	v_lshl_add_u64 v[182:183], v[186:187], 0, s[18:19]
	s_mov_b32 m0, s76
	s_nop 0
	global_load_lds_dwordx4 v[182:183], off
	s_waitcnt vmcnt(8)
	s_waitcnt lgkmcnt(0)
	s_setprio 1
	s_barrier
	v_mfma_f32_16x16x128_f8f6f4 v[94:97], v[2:9], v[208:215], v[94:97]
	v_mfma_f32_16x16x128_f8f6f4 v[90:93], v[10:17], v[208:215], v[90:93]
	v_mfma_f32_16x16x128_f8f6f4 v[78:81], v[2:9], v[216:223], v[78:81]
	v_mfma_f32_16x16x128_f8f6f4 v[74:77], v[10:17], v[216:223], v[74:77]
	v_mfma_f32_16x16x128_f8f6f4 v[58:61], v[2:9], v[224:231], v[58:61]
	v_mfma_f32_16x16x128_f8f6f4 v[46:49], v[10:17], v[224:231], v[46:49]
	v_mfma_f32_16x16x128_f8f6f4 v[38:41], v[2:9], v[232:239], v[38:41]
	v_mfma_f32_16x16x128_f8f6f4 v[34:37], v[10:17], v[232:239], v[34:37]
	v_mfma_f32_16x16x128_f8f6f4 v[86:89], v[18:25], v[208:215], v[86:89]
	v_mfma_f32_16x16x128_f8f6f4 v[82:85], v[26:33], v[208:215], v[82:85]
	v_mfma_f32_16x16x128_f8f6f4 v[62:65], v[18:25], v[216:223], v[62:65]
	v_mfma_f32_16x16x128_f8f6f4 v[54:57], v[26:33], v[216:223], v[54:57]
	v_mfma_f32_16x16x128_f8f6f4 v[70:73], v[18:25], v[224:231], v[70:73]
	v_mfma_f32_16x16x128_f8f6f4 v[66:69], v[26:33], v[224:231], v[66:69]
	v_mfma_f32_16x16x128_f8f6f4 v[50:53], v[18:25], v[232:239], v[50:53]
	v_mfma_f32_16x16x128_f8f6f4 v[42:45], v[26:33], v[232:239], v[42:45]
	s_setprio 0
	s_barrier
	s_add_i32 s49, s49, 2
	s_add_u32 s50, s50, 0x100
	s_addc_u32 s51, s51, 0
	s_cmp_gt_u32 s49, 13
	s_cbranch_scc0 .LBB0_1329
	s_and_b64 vcc, exec, s[38:39]
	s_cbranch_vccz .LBB0_1332
	s_barrier
